# v16 + P2: relaxed first two vmcnt waits of each unit after an epilogue; DOWN expert GEMM: MFMA operands swapped so the epilogue stores straight from registers (no LDS staging), loader prologue of next
# baseline (speedup 1.0000x reference)
; #define LAS __attribute__((address_space(3)))
; __global__ void __launch_bounds__(NTHR, 2) fwd_kernel(Args args) {
;     extern __shared__ __attribute__((aligned(16))) unsigned char lds_raw[];
;     LAS unsigned char* lds = (LAS unsigned char*)lds_raw;
;     const int tid = threadIdx.x, lane = tid & 63, wave = __builtin_amdgcn_readfirstlane(tid >> 6);
;     volatile LAS unsigned* MISC = (volatile LAS unsigned*)(lds + MISC_OFF);
;     if (tid < 64) MISC[tid] = 0u;
;     __syncthreads();
;     unsigned char* ws = args.ws;
;     unsigned* ctl = (unsigned*)(ws + WS_CTL);
;     XcdBarrier bar; bar.bar = ctl + CW_BAR; bar.x = 0; bar.st = nullptr;
;     if (N_LAUNCHES == 1) bar = xcd_barrier_post(ctl + CW_BAR, MISC + 8);
_Z10fwd_kernel4Args:
	s_mov_b32 s100, 0
	s_load_dwordx16 s[44:59], s[0:1], 0x80
	s_load_dwordx2 s[92:93], s[0:1], 0xc0
	s_mov_b32 s74, s2
	s_mov_b64 s[96:97], s[0:1]
	v_readfirstlane_b32 s0, v0
	v_cmp_gt_u32_e64 s[4:5], 64, v0
	s_nop 0
	v_writelane_b32 v244, s0, 0
	s_and_saveexec_b64 s[0:1], s[4:5]
	v_lshl_add_u32 v1, v0, 2, 0
	v_add_u32_e32 v1, 0x23f00, v1
	v_mov_b32_e32 v2, 0
	ds_write_b32 v1, v2
	s_or_b64 exec, exec, s[0:1]
	s_waitcnt lgkmcnt(0)
	s_add_u32 s0, s58, 0x4000
	s_addc_u32 s1, s59, 0
	v_writelane_b32 v244, s0, 1
	s_barrier
	s_nop 0
	v_writelane_b32 v244, s1, 2
	s_getreg_b32 s0, hwreg(HW_REG_XCC_ID, 0, 4)
	s_and_b32 s95, s0, 15
	v_cmp_eq_u32_e64 s[72:73], 0, v0
	s_and_saveexec_b64 s[0:1], s[72:73]
	s_cbranch_execz .LBB0_5
	s_mov_b64 s[6:7], exec
	v_mbcnt_lo_u32_b32 v1, s6, 0
	v_mbcnt_hi_u32_b32 v1, s7, v1
	v_cmp_eq_u32_e32 vcc, 0, v1
	s_and_b64 s[2:3], exec, vcc
	s_mov_b64 exec, s[2:3]
	s_cbranch_execz .LBB0_5
	s_lshl_b32 s2, s95, 8
	s_bcnt1_i32_b64 s3, s[6:7]
	v_mov_b32_e32 v1, s2
	v_mov_b32_e32 v2, s3
	v_readlane_b32 s2, v244, 1
	v_readlane_b32 s3, v244, 2
	s_nop 4
	global_atomic_add v1, v2, s[2:3] offset:1024

; #define PG8_STAGE(bufoff, gbase, voff) do { _Pragma("unroll") for (int _i = 0; _i < 2; ++_i) \
;         __builtin_amdgcn_global_load_lds((const unsigned*)((const char*)(gbase) + (voff)[_i]), (PG8_LAS unsigned*)(lds + (bufoff) + ldsw + _i * 8192), 16, 0, 0); } while (0)
; #define PG8_WAIT_V(n) asm volatile("s_waitcnt vmcnt(" #n ")" ::: "memory")
; #define PG8_BAR __builtin_amdgcn_s_barrier()
; template <class Epi, class Sched, bool ALIGN_EPI = false, bool SP2 = false>
; __device__ __forceinline__ void gemm_phase(PG8_LAS unsigned char* lds, const Gemm g, const Sched& S, const Epi& E) {
;     ...
;     for (int i = 0; i < 2; ++i) { int R, C; stage_rc(tid * 16 + i * 8192, R, C); const int Rb = Epi::PERM ? ((R & ~31) + perm32(R & 31)) : R;
;         voffA[i] = (unsigned)(R * K + C) * 2u; voffB[i] = (unsigned)(Rb * K + C) * 2u; }
;     const size_t kstep = (size_t)(BK * 2);
;     const size_t hstep = (size_t)HALF * K * 2;
;     const size_t tstep = 2 * hstep;
;     const unsigned ldsw = (unsigned)wid * 1024u;
;     const int aoff = lds_byte(wr * 64 + fr, fq * 8), boff = lds_byte(wc * 32 + fr, fq * 8);
;     ...
;         PG8_STAGE(PG8_SB(1, 0), cB + kstep, voffB); PG8_STAGE(PG8_SA(1, 0), cA + kstep, voffA); PG8_STAGE(PG8_SB(1, 1), cB + hstep + kstep, voffB);
;         PG8_WAIT_V(6); PG8_BAR;
;     } else {
;         PG8_STAGE(PG8_SB(0, 0), cB, voffB); PG8_STAGE(PG8_SA(0, 0), cA, voffA); PG8_STAGE(PG8_SB(0, 1), cB + hstep, voffB); PG8_STAGE(PG8_SA(0, 1), cA + hstep, voffA);
;         if (wr == 1) PG8_BAR;
;         PG8_WAIT_V(4); PG8_BAR;
;         PG8_STAGE(PG8_SB(1, 0), cB + kstep, voffB); PG8_STAGE(PG8_SA(1, 0), cA + kstep, voffA); PG8_STAGE(PG8_SB(1, 1), cB + hstep + kstep, voffB);
;         PG8_WAIT_V(6); PG8_BAR;
;     }
.LBB0_248:
	s_and_b32 s9, s7, 3
	s_lshl_b32 s20, s10, 13
	s_lshl_b32 s24, s9, 5
	s_lshl_b32 s9, s9, 12
	s_add_u32 s14, s58, 0x5000000
	s_addc_u32 s15, s59, 0
	s_add_u32 s25, s58, 0x6000000
	s_addc_u32 s37, s59, 0
	s_add_u32 s72, s58, 0x6400000
	s_addc_u32 s73, s59, 0
	s_add_u32 s16, s58, 0x6800000
	s_addc_u32 s17, s59, 0
	v_writelane_b32 v244, s16, 15
	s_mov_b64 s[28:29], 0x80
	v_lshl_add_u64 v[8:9], v[8:9], 0, s[28:29]
	v_writelane_b32 v244, s17, 16
	s_add_u32 s16, s58, 0x7800000
	s_addc_u32 s17, s59, 0
	v_writelane_b32 v244, s16, 17
	s_waitcnt vmcnt(2)
	s_barrier
	v_lshl_add_u64 v[6:7], v[6:7], 0, s[28:29]
	v_writelane_b32 v244, s17, 18
	s_add_u32 s16, s58, 0x8800000
	s_addc_u32 s17, s59, 0
	v_writelane_b32 v244, s16, 19
	v_lshl_add_u64 v[2:3], v[2:3], 0, s[28:29]
	v_mov_b32_e32 v159, v151
	v_writelane_b32 v244, s17, 20
	s_add_u32 s16, s58, 0x9800000
	s_addc_u32 s17, s59, 0
	s_add_i32 m0, s18, 0x18000
	v_writelane_b32 v244, s16, 21
	global_load_lds_dwordx4 v[8:9], off
	s_add_i32 m0, s18, 0x1a000
	s_add_i32 s23, s18, 0x8000
	s_add_i32 s26, s18, 0xa000
	v_writelane_b32 v244, s17, 22
	global_load_lds_dwordx4 v[6:7], off
	s_mov_b32 m0, s23
	s_add_u32 s16, s94, 0x80080
	global_load_lds_dwordx4 v[2:3], off
	v_lshl_add_u64 v[2:3], v[4:5], 0, s[28:29]
	s_mov_b32 m0, s26
	s_addc_u32 s17, s95, 0
	global_load_lds_dwordx4 v[2:3], off
	s_add_i32 m0, s18, 0x1c000
	v_lshl_add_u64 v[2:3], s[16:17], 0, v[146:147]
	global_load_lds_dwordx4 v[2:3], off
	v_lshl_add_u64 v[2:3], s[16:17], 0, v[148:149]
	s_add_i32 m0, s18, 0x1e000
	v_and_b32_e32 v5, 32, v1
	global_load_lds_dwordx4 v[2:3], off
	v_bfe_u32 v3, v0, 4, 2
	v_and_b32_e32 v2, 15, v0
	v_lshlrev_b32_e32 v4, 4, v3
	v_lshl_or_b32 v153, s10, 6, v2
	v_lshl_or_b32 v2, v2, 6, v4
	v_bitop3_b32 v6, v2, s20, v5 bitop3:0xde
	v_lshlrev_b32_e32 v2, 6, v0
	s_movk_i32 s10, 0x3c0
	v_and_or_b32 v2, v2, s10, v4
	s_cmpk_lt_u32 s6, 0x100
	v_bitop3_b32 v174, s9, v2, v5 bitop3:0xf6
	s_cselect_b64 s[30:31], -1, 0
	v_lshlrev_b32_e32 v2, 2, v3
	s_lshl_b32 s6, s7, 4
	v_and_or_b32 v152, s6, 16, v2
	s_lshl_b32 s6, s7, 5
	v_lshlrev_b32_e32 v150, 2, v152
	s_and_b32 s27, s6, 64
	v_lshl_add_u64 v[4:5], s[58:59], 0, v[150:151]
	s_mov_b64 s[6:7], 0x400000
	v_lshl_add_u64 v[154:155], v[4:5], 0, s[6:7]
	s_mov_b64 s[6:7], 0x500000
	v_lshlrev_b32_e32 v3, 9, v0
	s_lshl_b32 s9, s27, 1
	s_ashr_i32 s20, s43, 31
	s_ashr_i32 s21, s74, 31
	v_lshl_add_u64 v[156:157], v[4:5], 0, s[6:7]
	v_and_b32_e32 v3, 0x30000, v3
	v_lshlrev_b32_e32 v4, 12, v12
	s_add_u32 s34, s25, s9
	v_or3_b32 v3, v10, v3, v4
	s_addc_u32 s35, s37, 0
	s_bitset1_b32 s9, 8
	v_add_u32_e32 v158, v3, v11
	v_lshlrev_b32_e32 v3, 5, v13
	s_waitcnt vmcnt(6)
	s_add_u32 s36, s25, s9
	v_and_b32_e32 v3, 0x70000, v3
	s_addc_u32 s37, s37, 0
	v_or3_b32 v3, v10, v3, v4
	s_add_i32 s42, 0, 0x10000
	s_add_i32 s16, 0, 0x14000
	v_or_b32_e32 v176, 16, v153
	v_or_b32_e32 v177, 32, v153
	v_or_b32_e32 v178, 48, v153
	v_add_u32_e32 v179, 0x80, v153
	v_add_u32_e32 v180, 0x90, v153
	v_add_u32_e32 v181, 0xa0, v153
	v_add_u32_e32 v182, 0xb0, v153
	v_add_u32_e32 v160, v3, v11
	v_mov_b32_e32 v161, v151
	v_mov_b64_e32 v[162:163], 0x2c0
	v_mov_b64_e32 v[164:165], 0x2bf
	s_mov_b64 s[40:41], 0x100
	v_add_u32_e32 v183, s42, v174
	v_add_u32_e32 v184, s16, v174
	v_add_u32_e32 v185, 0, v6
	s_lshl_b32 s17, s24, 1
	v_lshlrev_b32_e32 v166, 1, v2
	s_mov_b32 s68, 0x3e000000
	s_mov_b32 s60, 0
	s_barrier
	s_branch .LBB0_251
	s_mov_b32 s99, 0

; #define PG8_STAGE(bufoff, gbase, voff) do { _Pragma("unroll") for (int _i = 0; _i < 2; ++_i) \
;         __builtin_amdgcn_global_load_lds((const unsigned*)((const char*)(gbase) + (voff)[_i]), (PG8_LAS unsigned*)(lds + (bufoff) + ldsw + _i * 8192), 16, 0, 0); } while (0)
; #define PG8_LDA(dst, b, h) do { _Pragma("unroll") for (int m = 0; m < 4; ++m) _Pragma("unroll") for (int k = 0; k < 2; ++k) dst[m][k] = *(const PG8_LAS bf16x8*)(lds + PG8_SA(b, h) + aoff + m * 2048 + k * 1024); } while (0)
; #define PG8_LDB(dst, b, h) do { _Pragma("unroll") for (int n = 0; n < 2; ++n) _Pragma("unroll") for (int k = 0; k < 2; ++k) dst[n][k] = *(const PG8_LAS bf16x8*)(lds + PG8_SB(b, h) + boff + n * 2048 + k * 1024); } while (0)
; #define PG8_MMA(ai, bj, At, Bt) do { __builtin_amdgcn_s_setprio(1); _Pragma("unroll") for (int m = 0; m < 4; ++m) _Pragma("unroll") for (int n = 0; n < 2; ++n) _Pragma("unroll") for (int k = 0; k < 2; ++k) \
;         acc[ai][bj][m][n] = __builtin_amdgcn_mfma_f32_16x16x32_bf16(Bt[n][k], At[m][k], acc[ai][bj][m][n], 0, 0, 0); __builtin_amdgcn_s_setprio(0); } while (0)
; #define PG8_WAIT_V(n) asm volatile("s_waitcnt vmcnt(" #n ")" ::: "memory")
; #define PG8_BAR __builtin_amdgcn_s_barrier()
; template <class Epi, class Sched, bool ALIGN_EPI = false, bool SP2 = false>
; __device__ __forceinline__ void gemm_phase(PG8_LAS unsigned char* lds, const Gemm g, const Sched& S, const Epi& E) {
;     ...
;         for (int t = 0; t < nt; t += 2) {
;             const bool last = (t == nt - 2);
;             const char* a1 = cA + (size_t)(t + 1) * kstep;
;             const char* a2 = last ? nA : cA + (size_t)(t + 2) * kstep; const char* b2 = last ? nB : cB + (size_t)(t + 2) * kstep;
;             const char* a3 = a2 + kstep; const char* b3 = b2 + kstep;
;             if (last && has_next) S.a_ready(nxt);
;             if constexpr (SP2) {
;             PG8_LDB(B0, 0, 0); PG8_LDB(B1, 0, 1); PG8_SCHED; PG8_LDA(At, 0, 0); PG8_STAGE(PG8_SA(1, 1), a1 + hstep, voffA);
;             PG8_WAIT_V(8); PG8_WAIT_L(0); PG8_BAR; PG8_MMA(0, 0, At, B0); PG8_MMA(0, 1, At, B1); PG8_BAR; PG8_SCHED;
;             PG8_LDA(At, 0, 1); PG8_STAGE(PG8_SB(0, 0), b2, voffB); PG8_STAGE(PG8_SB(0, 1), b2 + hstep, voffB); PG8_STAGE(PG8_SA(0, 0), a2, voffA);
;             PG8_WAIT_V(8); PG8_WAIT_L(0); PG8_BAR; PG8_MMA(1, 0, At, B0); PG8_MMA(1, 1, At, B1); PG8_BAR; PG8_SCHED;
.LBB0_254:
	ds_read_b128 v[130:133], v183
	ds_read_b128 v[134:137], v183 offset:1024
	ds_read_b128 v[138:141], v183 offset:2048
	ds_read_b128 v[142:145], v183 offset:3072
	ds_read_b128 v[168:171], v184
	ds_read_b128 v[186:189], v184 offset:1024
	ds_read_b128 v[190:193], v184 offset:2048
	ds_read_b128 v[194:197], v184 offset:3072
	s_cmp_eq_u32 s64, -2
	s_cselect_b32 s98, s99, 0
	s_add_u32 s65, vcc_lo, 0xfff80080
	s_addc_u32 s66, vcc_hi, -1
	s_cmp_eq_u32 s64, 28
	s_cselect_b32 s97, s9, s66
	s_cselect_b32 s96, s10, s65
	s_cselect_b32 s95, s39, s63
	s_cselect_b32 s94, s61, s62
	v_lshl_add_u64 v[172:173], vcc, 0, v[158:159]
	s_add_i32 m0, s18, 0xc000
	ds_read_b128 v[198:201], v185
	ds_read_b128 v[202:205], v185 offset:1024
	ds_read_b128 v[206:209], v185 offset:2048
	ds_read_b128 v[210:213], v185 offset:3072
	ds_read_b128 v[214:217], v185 offset:4096
	ds_read_b128 v[218:221], v185 offset:5120
	ds_read_b128 v[222:225], v185 offset:6144
	ds_read_b128 v[226:229], v185 offset:7168
	global_load_lds_dwordx4 v[172:173], off
	v_lshl_add_u64 v[172:173], vcc, 0, v[160:161]
	s_add_i32 m0, s18, 0xe000
	s_nop 0
	global_load_lds_dwordx4 v[172:173], off
	s_cmp_lg_u32 s98, 0
	s_cbranch_scc1 .Lp2_wrelaxA
	s_waitcnt vmcnt(8)
	s_branch .Lp2_wdoneA
.Lp2_wrelaxA:
	s_waitcnt vmcnt(24)
.Lp2_wdoneA:
	s_waitcnt lgkmcnt(0)
	s_barrier
	s_setprio 1
	s_waitcnt lgkmcnt(0)
	v_mfma_f32_16x16x32_bf16 v[126:129], v[130:133], v[198:201], v[126:129]
	v_mfma_f32_16x16x32_bf16 v[122:125], v[138:141], v[198:201], v[122:125]
	v_mfma_f32_16x16x32_bf16 v[110:113], v[130:133], v[206:209], v[110:113]
	v_mfma_f32_16x16x32_bf16 v[106:109], v[138:141], v[206:209], v[106:109]
	v_mfma_f32_16x16x32_bf16 v[94:97], v[130:133], v[214:217], v[94:97]
	v_mfma_f32_16x16x32_bf16 v[90:93], v[138:141], v[214:217], v[90:93]
	v_mfma_f32_16x16x32_bf16 v[78:81], v[130:133], v[222:225], v[78:81]
	v_mfma_f32_16x16x32_bf16 v[74:77], v[138:141], v[222:225], v[74:77]
	v_mfma_f32_16x16x32_bf16 v[126:129], v[134:137], v[202:205], v[126:129]
	v_mfma_f32_16x16x32_bf16 v[122:125], v[142:145], v[202:205], v[122:125]
	v_mfma_f32_16x16x32_bf16 v[110:113], v[134:137], v[210:213], v[110:113]
	v_mfma_f32_16x16x32_bf16 v[106:109], v[142:145], v[210:213], v[106:109]
	v_mfma_f32_16x16x32_bf16 v[94:97], v[134:137], v[218:221], v[94:97]
	v_mfma_f32_16x16x32_bf16 v[90:93], v[142:145], v[218:221], v[90:93]
	v_mfma_f32_16x16x32_bf16 v[78:81], v[134:137], v[226:229], v[78:81]
	v_mfma_f32_16x16x32_bf16 v[74:77], v[142:145], v[226:229], v[74:77]
	s_setprio 0
	s_setprio 1
	v_mfma_f32_16x16x32_bf16 v[118:121], v[168:171], v[198:201], v[118:121]
	v_mfma_f32_16x16x32_bf16 v[114:117], v[190:193], v[198:201], v[114:117]
	v_mfma_f32_16x16x32_bf16 v[102:105], v[168:171], v[206:209], v[102:105]
	v_mfma_f32_16x16x32_bf16 v[98:101], v[190:193], v[206:209], v[98:101]
	v_mfma_f32_16x16x32_bf16 v[86:89], v[168:171], v[214:217], v[86:89]
	v_mfma_f32_16x16x32_bf16 v[82:85], v[190:193], v[214:217], v[82:85]
	v_mfma_f32_16x16x32_bf16 v[70:73], v[168:171], v[222:225], v[70:73]
	v_mfma_f32_16x16x32_bf16 v[66:69], v[190:193], v[222:225], v[66:69]
	v_mfma_f32_16x16x32_bf16 v[118:121], v[186:189], v[202:205], v[118:121]
	v_mfma_f32_16x16x32_bf16 v[114:117], v[194:197], v[202:205], v[114:117]
	v_mfma_f32_16x16x32_bf16 v[102:105], v[186:189], v[210:213], v[102:105]
	v_mfma_f32_16x16x32_bf16 v[98:101], v[194:197], v[210:213], v[98:101]
	v_mfma_f32_16x16x32_bf16 v[86:89], v[186:189], v[218:221], v[86:89]
	v_mfma_f32_16x16x32_bf16 v[82:85], v[194:197], v[218:221], v[82:85]
	v_mfma_f32_16x16x32_bf16 v[70:73], v[186:189], v[226:229], v[70:73]
	v_mfma_f32_16x16x32_bf16 v[66:69], v[194:197], v[226:229], v[66:69]
	s_setprio 0
	s_barrier
	s_add_i32 s65, s42, s2
	v_lshl_add_u64 v[172:173], s[94:95], 0, v[146:147]
	s_mov_b32 m0, s65
	ds_read_b128 v[198:201], v185 offset:16384
	ds_read_b128 v[202:205], v185 offset:17408
	ds_read_b128 v[206:209], v185 offset:18432
	ds_read_b128 v[210:213], v185 offset:19456
	ds_read_b128 v[214:217], v185 offset:20480
	ds_read_b128 v[218:221], v185 offset:21504
	ds_read_b128 v[222:225], v185 offset:22528
	ds_read_b128 v[226:229], v185 offset:23552
	global_load_lds_dwordx4 v[172:173], off
	s_add_i32 m0, s65, 0x2000
	s_add_u32 s66, s94, 0x80000
	v_lshl_add_u64 v[230:231], s[94:95], 0, v[148:149]
	s_addc_u32 s67, s95, 0
	s_add_i32 s65, s16, s2
	global_load_lds_dwordx4 v[230:231], off
	v_lshl_add_u64 v[232:233], s[66:67], 0, v[146:147]
	s_mov_b32 m0, s65
	v_lshl_add_u64 v[234:235], s[96:97], 0, v[148:149]
	global_load_lds_dwordx4 v[232:233], off
	v_lshl_add_u64 v[232:233], s[66:67], 0, v[148:149]
	s_add_i32 m0, s65, 0x2000
	s_nop 0
	global_load_lds_dwordx4 v[232:233], off
	v_lshl_add_u64 v[232:233], s[96:97], 0, v[146:147]
	s_mov_b32 m0, s18
	s_nop 0
	global_load_lds_dwordx4 v[232:233], off
	s_mov_b32 m0, s19
	s_nop 0
	global_load_lds_dwordx4 v[234:235], off
	s_cmp_lg_u32 s98, 0
	s_cbranch_scc1 .Lp2_wrelaxB
	s_waitcnt vmcnt(8)
	s_branch .Lp2_wdoneB

; #define PG8_STAGE(bufoff, gbase, voff) do { _Pragma("unroll") for (int _i = 0; _i < 2; ++_i) \
;         __builtin_amdgcn_global_load_lds((const unsigned*)((const char*)(gbase) + (voff)[_i]), (PG8_LAS unsigned*)(lds + (bufoff) + ldsw + _i * 8192), 16, 0, 0); } while (0)
; #define PG8_LDA(dst, b, h) do { _Pragma("unroll") for (int m = 0; m < 4; ++m) _Pragma("unroll") for (int k = 0; k < 2; ++k) dst[m][k] = *(const PG8_LAS bf16x8*)(lds + PG8_SA(b, h) + aoff + m * 2048 + k * 1024); } while (0)
; #define PG8_LDB(dst, b, h) do { _Pragma("unroll") for (int n = 0; n < 2; ++n) _Pragma("unroll") for (int k = 0; k < 2; ++k) dst[n][k] = *(const PG8_LAS bf16x8*)(lds + PG8_SB(b, h) + boff + n * 2048 + k * 1024); } while (0)
; #define PG8_MMA(ai, bj, At, Bt) do { __builtin_amdgcn_s_setprio(1); _Pragma("unroll") for (int m = 0; m < 4; ++m) _Pragma("unroll") for (int n = 0; n < 2; ++n) _Pragma("unroll") for (int k = 0; k < 2; ++k) \
;         acc[ai][bj][m][n] = __builtin_amdgcn_mfma_f32_16x16x32_bf16(Bt[n][k], At[m][k], acc[ai][bj][m][n], 0, 0, 0); __builtin_amdgcn_s_setprio(0); } while (0)
; #define PG8_WAIT_V(n) asm volatile("s_waitcnt vmcnt(" #n ")" ::: "memory")
; #define PG8_WAIT_L(n) asm volatile("s_waitcnt lgkmcnt(" #n ")" ::: "memory")
; #define PG8_BAR __builtin_amdgcn_s_barrier()
; #define PG8_SCHED __builtin_amdgcn_sched_barrier(0)
; template <class Epi, class Sched, bool ALIGN_EPI = false, bool SP2 = false>
; __device__ __forceinline__ void gemm_phase(PG8_LAS unsigned char* lds, const Gemm g, const Sched& S, const Epi& E) {
;     ...
;             PG8_WAIT_V(8); PG8_WAIT_L(0); PG8_BAR; PG8_MMA(1, 0, At, B0); PG8_MMA(1, 1, At, B1); PG8_BAR; PG8_SCHED;
;             PG8_LDB(B0, 1, 0); PG8_LDB(B1, 1, 1); PG8_SCHED; PG8_LDA(At, 1, 0); PG8_STAGE(PG8_SA(0, 1), a2 + hstep, voffA);
;             PG8_WAIT_V(8); PG8_WAIT_L(0); PG8_BAR; PG8_MMA(0, 0, At, B0); PG8_MMA(0, 1, At, B1); PG8_BAR; PG8_SCHED;
;             PG8_LDA(At, 1, 1); PG8_STAGE(PG8_SB(1, 0), b3, voffB); PG8_STAGE(PG8_SB(1, 1), b3 + hstep, voffB); PG8_STAGE(PG8_SA(1, 0), a3, voffA);
.Lp2_wdoneB:
	s_waitcnt lgkmcnt(0)
	s_barrier
	s_setprio 1
	s_waitcnt lgkmcnt(0)
	v_mfma_f32_16x16x32_bf16 v[62:65], v[130:133], v[198:201], v[62:65]
	v_mfma_f32_16x16x32_bf16 v[58:61], v[138:141], v[198:201], v[58:61]
	v_mfma_f32_16x16x32_bf16 v[46:49], v[130:133], v[206:209], v[46:49]
	v_mfma_f32_16x16x32_bf16 v[42:45], v[138:141], v[206:209], v[42:45]
	v_mfma_f32_16x16x32_bf16 v[30:33], v[130:133], v[214:217], v[30:33]
	v_mfma_f32_16x16x32_bf16 v[26:29], v[138:141], v[214:217], v[26:29]
	v_mfma_f32_16x16x32_bf16 v[14:17], v[130:133], v[222:225], v[14:17]
	v_mfma_f32_16x16x32_bf16 v[10:13], v[138:141], v[222:225], v[10:13]
	v_mfma_f32_16x16x32_bf16 v[62:65], v[134:137], v[202:205], v[62:65]
	v_mfma_f32_16x16x32_bf16 v[58:61], v[142:145], v[202:205], v[58:61]
	v_mfma_f32_16x16x32_bf16 v[46:49], v[134:137], v[210:213], v[46:49]
	v_mfma_f32_16x16x32_bf16 v[42:45], v[142:145], v[210:213], v[42:45]
	v_mfma_f32_16x16x32_bf16 v[30:33], v[134:137], v[218:221], v[30:33]
	v_mfma_f32_16x16x32_bf16 v[26:29], v[142:145], v[218:221], v[26:29]
	v_mfma_f32_16x16x32_bf16 v[14:17], v[134:137], v[226:229], v[14:17]
	v_mfma_f32_16x16x32_bf16 v[10:13], v[142:145], v[226:229], v[10:13]
	s_setprio 0
	s_setprio 1
	v_mfma_f32_16x16x32_bf16 v[54:57], v[168:171], v[198:201], v[54:57]
	v_mfma_f32_16x16x32_bf16 v[50:53], v[190:193], v[198:201], v[50:53]
	v_mfma_f32_16x16x32_bf16 v[38:41], v[168:171], v[206:209], v[38:41]
	v_mfma_f32_16x16x32_bf16 v[34:37], v[190:193], v[206:209], v[34:37]
	v_mfma_f32_16x16x32_bf16 v[22:25], v[168:171], v[214:217], v[22:25]
	v_mfma_f32_16x16x32_bf16 v[18:21], v[190:193], v[214:217], v[18:21]
	v_mfma_f32_16x16x32_bf16 v[6:9], v[168:171], v[222:225], v[6:9]
	v_mfma_f32_16x16x32_bf16 v[2:5], v[190:193], v[222:225], v[2:5]
	v_mfma_f32_16x16x32_bf16 v[54:57], v[186:189], v[202:205], v[54:57]
	v_mfma_f32_16x16x32_bf16 v[50:53], v[194:197], v[202:205], v[50:53]
	v_mfma_f32_16x16x32_bf16 v[38:41], v[186:189], v[210:213], v[38:41]
	v_mfma_f32_16x16x32_bf16 v[34:37], v[194:197], v[210:213], v[34:37]
	v_mfma_f32_16x16x32_bf16 v[22:25], v[186:189], v[218:221], v[22:25]
	v_mfma_f32_16x16x32_bf16 v[18:21], v[194:197], v[218:221], v[18:21]
	v_mfma_f32_16x16x32_bf16 v[6:9], v[186:189], v[226:229], v[6:9]
	v_mfma_f32_16x16x32_bf16 v[2:5], v[194:197], v[226:229], v[2:5]
	s_setprio 0
	s_barrier
	s_add_i32 s65, 0, 0x18000
	s_add_i32 s70, 0, 0x1c000
	v_add_u32_e32 v142, s65, v174
	v_add_u32_e32 v150, s70, v174
	ds_read_b128 v[130:133], v142
	ds_read_b128 v[134:137], v142 offset:1024
	ds_read_b128 v[138:141], v142 offset:2048
	ds_read_b128 v[142:145], v142 offset:3072
	ds_read_b128 v[168:171], v150
	ds_read_b128 v[186:189], v150 offset:1024
	ds_read_b128 v[190:193], v150 offset:2048
	ds_read_b128 v[194:197], v150 offset:3072
	s_add_u32 s66, s96, 0x80000
	s_addc_u32 s67, s97, 0
	s_mov_b32 m0, s3
	v_lshl_add_u64 v[236:237], s[66:67], 0, v[146:147]
	ds_read_b128 v[198:201], v185 offset:32768
	ds_read_b128 v[202:205], v185 offset:33792
	ds_read_b128 v[206:209], v185 offset:34816
	ds_read_b128 v[210:213], v185 offset:35840
	ds_read_b128 v[214:217], v185 offset:36864
	ds_read_b128 v[218:221], v185 offset:37888
	ds_read_b128 v[222:225], v185 offset:38912
	ds_read_b128 v[226:229], v185 offset:39936
	global_load_lds_dwordx4 v[236:237], off
	v_lshl_add_u64 v[236:237], s[66:67], 0, v[148:149]
	s_mov_b32 m0, s22
	s_nop 0
	global_load_lds_dwordx4 v[236:237], off
	s_waitcnt vmcnt(8)
	s_waitcnt lgkmcnt(0)
	s_barrier
	s_setprio 1
	s_waitcnt lgkmcnt(0)
	v_mfma_f32_16x16x32_bf16 v[126:129], v[130:133], v[198:201], v[126:129]
	v_mfma_f32_16x16x32_bf16 v[122:125], v[138:141], v[198:201], v[122:125]
	v_mfma_f32_16x16x32_bf16 v[110:113], v[130:133], v[206:209], v[110:113]
	v_mfma_f32_16x16x32_bf16 v[106:109], v[138:141], v[206:209], v[106:109]
	v_mfma_f32_16x16x32_bf16 v[94:97], v[130:133], v[214:217], v[94:97]
	v_mfma_f32_16x16x32_bf16 v[90:93], v[138:141], v[214:217], v[90:93]
	v_mfma_f32_16x16x32_bf16 v[78:81], v[130:133], v[222:225], v[78:81]
	v_mfma_f32_16x16x32_bf16 v[74:77], v[138:141], v[222:225], v[74:77]
	v_mfma_f32_16x16x32_bf16 v[126:129], v[134:137], v[202:205], v[126:129]
	v_mfma_f32_16x16x32_bf16 v[122:125], v[142:145], v[202:205], v[122:125]
	v_mfma_f32_16x16x32_bf16 v[110:113], v[134:137], v[210:213], v[110:113]
	v_mfma_f32_16x16x32_bf16 v[106:109], v[142:145], v[210:213], v[106:109]
	v_mfma_f32_16x16x32_bf16 v[94:97], v[134:137], v[218:221], v[94:97]
	v_mfma_f32_16x16x32_bf16 v[90:93], v[142:145], v[218:221], v[90:93]
	v_mfma_f32_16x16x32_bf16 v[78:81], v[134:137], v[226:229], v[78:81]
	v_mfma_f32_16x16x32_bf16 v[74:77], v[142:145], v[226:229], v[74:77]
	s_setprio 0
	s_setprio 1
	v_mfma_f32_16x16x32_bf16 v[118:121], v[168:171], v[198:201], v[118:121]
	v_mfma_f32_16x16x32_bf16 v[114:117], v[190:193], v[198:201], v[114:117]
	v_mfma_f32_16x16x32_bf16 v[102:105], v[168:171], v[206:209], v[102:105]
	v_mfma_f32_16x16x32_bf16 v[98:101], v[190:193], v[206:209], v[98:101]
	v_mfma_f32_16x16x32_bf16 v[86:89], v[168:171], v[214:217], v[86:89]
	v_mfma_f32_16x16x32_bf16 v[82:85], v[190:193], v[214:217], v[82:85]
	v_mfma_f32_16x16x32_bf16 v[70:73], v[168:171], v[222:225], v[70:73]
	v_mfma_f32_16x16x32_bf16 v[66:69], v[190:193], v[222:225], v[66:69]
	v_mfma_f32_16x16x32_bf16 v[118:121], v[186:189], v[202:205], v[118:121]
	v_mfma_f32_16x16x32_bf16 v[114:117], v[194:197], v[202:205], v[114:117]
	v_mfma_f32_16x16x32_bf16 v[102:105], v[186:189], v[210:213], v[102:105]
	v_mfma_f32_16x16x32_bf16 v[98:101], v[194:197], v[210:213], v[98:101]
	v_mfma_f32_16x16x32_bf16 v[86:89], v[186:189], v[218:221], v[86:89]
	v_mfma_f32_16x16x32_bf16 v[82:85], v[194:197], v[218:221], v[82:85]
	v_mfma_f32_16x16x32_bf16 v[70:73], v[186:189], v[226:229], v[70:73]
	v_mfma_f32_16x16x32_bf16 v[66:69], v[194:197], v[226:229], v[66:69]
	s_setprio 0
	s_barrier
; #define PG8_STAGE(bufoff, gbase, voff) do { _Pragma("unroll") for (int _i = 0; _i < 2; ++_i) \
;         __builtin_amdgcn_global_load_lds((const unsigned*)((const char*)(gbase) + (voff)[_i]), (PG8_LAS unsigned*)(lds + (bufoff) + ldsw + _i * 8192), 16, 0, 0); } while (0)
; #define PG8_LDA(dst, b, h) do { _Pragma("unroll") for (int m = 0; m < 4; ++m) _Pragma("unroll") for (int k = 0; k < 2; ++k) dst[m][k] = *(const PG8_LAS bf16x8*)(lds + PG8_SA(b, h) + aoff + m * 2048 + k * 1024); } while (0)
; #define PG8_MMA(ai, bj, At, Bt) do { __builtin_amdgcn_s_setprio(1); _Pragma("unroll") for (int m = 0; m < 4; ++m) _Pragma("unroll") for (int n = 0; n < 2; ++n) _Pragma("unroll") for (int k = 0; k < 2; ++k) \
;         acc[ai][bj][m][n] = __builtin_amdgcn_mfma_f32_16x16x32_bf16(Bt[n][k], At[m][k], acc[ai][bj][m][n], 0, 0, 0); __builtin_amdgcn_s_setprio(0); } while (0)
; #define PG8_WAIT_V(n) asm volatile("s_waitcnt vmcnt(" #n ")" ::: "memory")
; #define PG8_WAIT_L(n) asm volatile("s_waitcnt lgkmcnt(" #n ")" ::: "memory")
; #define PG8_BAR __builtin_amdgcn_s_barrier()
; #define PG8_SCHED __builtin_amdgcn_sched_barrier(0)
; template <class Epi, class Sched, bool ALIGN_EPI = false, bool SP2 = false>
; __device__ __forceinline__ void gemm_phase(PG8_LAS unsigned char* lds, const Gemm g, const Sched& S, const Epi& E) {
;     ...
;         for (int t = 0; t < nt; t += 2) {
;     ...
;             PG8_LDA(At, 1, 1); PG8_STAGE(PG8_SB(1, 0), b3, voffB); PG8_STAGE(PG8_SB(1, 1), b3 + hstep, voffB); PG8_STAGE(PG8_SA(1, 0), a3, voffA);
;             PG8_WAIT_V(8); PG8_WAIT_L(0); PG8_BAR; PG8_MMA(1, 0, At, B0); PG8_MMA(1, 1, At, B1); PG8_BAR; PG8_SCHED;
	s_add_i32 s65, s65, s2
	v_lshl_add_u64 v[172:173], v[172:173], 0, s[28:29]
	s_mov_b32 m0, s65
	ds_read_b128 v[198:201], v185 offset:49152
	ds_read_b128 v[202:205], v185 offset:50176
	ds_read_b128 v[206:209], v185 offset:51200
	ds_read_b128 v[210:213], v185 offset:52224
	ds_read_b128 v[214:217], v185 offset:53248
	ds_read_b128 v[218:221], v185 offset:54272
	ds_read_b128 v[222:225], v185 offset:55296
	ds_read_b128 v[226:229], v185 offset:56320
	global_load_lds_dwordx4 v[172:173], off
	s_add_i32 m0, s65, 0x2000
	s_add_u32 s66, s94, 0x80080
	v_lshl_add_u64 v[172:173], v[230:231], 0, s[28:29]
	s_addc_u32 s67, s95, 0
	s_add_i32 s65, s70, s2
	global_load_lds_dwordx4 v[172:173], off
	v_lshl_add_u64 v[172:173], s[66:67], 0, v[146:147]
	s_mov_b32 m0, s65
	s_nop 0
	global_load_lds_dwordx4 v[172:173], off
	v_lshl_add_u64 v[172:173], s[66:67], 0, v[148:149]
	s_add_i32 m0, s65, 0x2000
	s_nop 0
	global_load_lds_dwordx4 v[172:173], off
	v_lshl_add_u64 v[172:173], v[232:233], 0, s[28:29]
	s_mov_b32 m0, s23
	s_nop 0
	global_load_lds_dwordx4 v[172:173], off
	v_lshl_add_u64 v[172:173], v[234:235], 0, s[28:29]
	s_mov_b32 m0, s26
	s_nop 0
	global_load_lds_dwordx4 v[172:173], off
	s_waitcnt vmcnt(8)
	s_waitcnt lgkmcnt(0)
	s_barrier
	s_setprio 1
	s_waitcnt lgkmcnt(0)
	v_mfma_f32_16x16x32_bf16 v[62:65], v[130:133], v[198:201], v[62:65]
	v_mfma_f32_16x16x32_bf16 v[58:61], v[138:141], v[198:201], v[58:61]
	v_mfma_f32_16x16x32_bf16 v[46:49], v[130:133], v[206:209], v[46:49]
	v_mfma_f32_16x16x32_bf16 v[42:45], v[138:141], v[206:209], v[42:45]
	v_mfma_f32_16x16x32_bf16 v[30:33], v[130:133], v[214:217], v[30:33]
	v_mfma_f32_16x16x32_bf16 v[26:29], v[138:141], v[214:217], v[26:29]
	v_mfma_f32_16x16x32_bf16 v[14:17], v[130:133], v[222:225], v[14:17]
	v_mfma_f32_16x16x32_bf16 v[10:13], v[138:141], v[222:225], v[10:13]
	v_mfma_f32_16x16x32_bf16 v[62:65], v[134:137], v[202:205], v[62:65]
	v_mfma_f32_16x16x32_bf16 v[58:61], v[142:145], v[202:205], v[58:61]
	v_mfma_f32_16x16x32_bf16 v[46:49], v[134:137], v[210:213], v[46:49]
	v_mfma_f32_16x16x32_bf16 v[42:45], v[142:145], v[210:213], v[42:45]
	v_mfma_f32_16x16x32_bf16 v[30:33], v[134:137], v[218:221], v[30:33]
	v_mfma_f32_16x16x32_bf16 v[26:29], v[142:145], v[218:221], v[26:29]
	v_mfma_f32_16x16x32_bf16 v[14:17], v[134:137], v[226:229], v[14:17]
	v_mfma_f32_16x16x32_bf16 v[10:13], v[142:145], v[226:229], v[10:13]
	s_setprio 0
	s_setprio 1
	v_mfma_f32_16x16x32_bf16 v[54:57], v[168:171], v[198:201], v[54:57]
	v_mfma_f32_16x16x32_bf16 v[50:53], v[190:193], v[198:201], v[50:53]
	v_mfma_f32_16x16x32_bf16 v[38:41], v[168:171], v[206:209], v[38:41]
	v_mfma_f32_16x16x32_bf16 v[34:37], v[190:193], v[206:209], v[34:37]
	v_mfma_f32_16x16x32_bf16 v[22:25], v[168:171], v[214:217], v[22:25]
	v_mfma_f32_16x16x32_bf16 v[18:21], v[190:193], v[214:217], v[18:21]
	v_mfma_f32_16x16x32_bf16 v[6:9], v[168:171], v[222:225], v[6:9]
	v_mfma_f32_16x16x32_bf16 v[2:5], v[190:193], v[222:225], v[2:5]
	v_mfma_f32_16x16x32_bf16 v[54:57], v[186:189], v[202:205], v[54:57]
	v_mfma_f32_16x16x32_bf16 v[50:53], v[194:197], v[202:205], v[50:53]
	v_mfma_f32_16x16x32_bf16 v[38:41], v[186:189], v[210:213], v[38:41]
	v_mfma_f32_16x16x32_bf16 v[34:37], v[194:197], v[210:213], v[34:37]
	v_mfma_f32_16x16x32_bf16 v[22:25], v[186:189], v[218:221], v[22:25]
	v_mfma_f32_16x16x32_bf16 v[18:21], v[194:197], v[218:221], v[18:21]
	v_mfma_f32_16x16x32_bf16 v[6:9], v[186:189], v[226:229], v[6:9]
	v_mfma_f32_16x16x32_bf16 v[2:5], v[194:197], v[226:229], v[2:5]
	s_setprio 0
	s_barrier
	s_add_i32 s64, s64, 2
	s_add_u32 vcc_lo, vcc_lo, 0x100
	s_addc_u32 vcc_hi, vcc_hi, 0
	s_add_u32 s62, s62, 0x100
	s_addc_u32 s63, s63, 0
	s_cmp_gt_u32 s64, 29
	s_cbranch_scc0 .LBB0_254
	s_and_b64 vcc, exec, s[30:31]
	s_cbranch_vccz .LBB0_323
	s_barrier
	s_cmp_gt_i32 s8, 4
	s_mov_b64 s[94:95], -1
	s_cbranch_scc1 .LBB0_324

; #define PG8_BAR __builtin_amdgcn_s_barrier()
; template <class Epi, class Sched, bool ALIGN_EPI = false, bool SP2 = false>
; __device__ __forceinline__ void gemm_phase(PG8_LAS unsigned char* lds, const Gemm g, const Sched& S, const Epi& E) {
;     ...
;         cur = nxt; cA = nA; cB = nB; ++ui;
;         if constexpr (ALIGN_EPI) { if (wr == 1) PG8_BAR; }
;     }
.LBB0_341:
	s_mov_b32 s99, 1
	s_andn2_b64 vcc, exec, s[12:13]
	s_cbranch_vccnz .LBB0_249
	s_barrier
	s_branch .LBB0_249

; template <bool UP>
; __device__ __forceinline__ void xgemm_unit(const Args& a, LAS unsigned char* lds, int e, int s, int cnt, int off_e, int rp, int tid, int lane, int wave) {
;     ...
;             __syncthreads();
; #pragma unroll 1
;             for (int t = 0; t < NK; t += 2) {
;                 XG_COMPUTE(0);
;                 __syncthreads();
;                 XG_COMPUTE(XG_BUF);
;                 __syncthreads();
;             }
.LBB0_1266:
	ds_read_b128 v[182:185], v163
	ds_read_b128 v[186:189], v163 offset:2560
	ds_read_b128 v[190:193], v163 offset:5120
	ds_read_b128 v[194:197], v163 offset:7680
	ds_read_b64_tr_b16 v[198:199], v164 offset:40960
	ds_read_b64_tr_b16 v[202:203], v164 offset:40992
	ds_read_b64_tr_b16 v[206:207], v164 offset:41024
	ds_read_b64_tr_b16 v[210:211], v164 offset:41056
	ds_read_b64_tr_b16 v[200:201], v164 offset:42048
	ds_read_b64_tr_b16 v[204:205], v164 offset:42080
	ds_read_b64_tr_b16 v[208:209], v164 offset:42112
	ds_read_b64_tr_b16 v[212:213], v164 offset:42144
	s_waitcnt lgkmcnt(3)
	v_mfma_f32_16x16x32_bf16 v[124:127], v[198:201], v[182:185], v[124:127]
	s_waitcnt lgkmcnt(2)
	v_mfma_f32_16x16x32_bf16 v[120:123], v[202:205], v[182:185], v[120:123]
	s_waitcnt lgkmcnt(1)
	v_mfma_f32_16x16x32_bf16 v[116:119], v[206:209], v[182:185], v[116:119]
	v_mfma_f32_16x16x32_bf16 v[92:95], v[198:201], v[186:189], v[92:95]
	v_mfma_f32_16x16x32_bf16 v[88:91], v[202:205], v[186:189], v[88:91]
	v_mfma_f32_16x16x32_bf16 v[84:87], v[206:209], v[186:189], v[84:87]
	v_mfma_f32_16x16x32_bf16 v[60:63], v[198:201], v[190:193], v[60:63]
	v_mfma_f32_16x16x32_bf16 v[56:59], v[202:205], v[190:193], v[56:59]
	v_mfma_f32_16x16x32_bf16 v[52:55], v[206:209], v[190:193], v[52:55]
	v_mfma_f32_16x16x32_bf16 v[24:27], v[198:201], v[194:197], v[24:27]
	ds_read_b64_tr_b16 v[198:199], v164 offset:41088
	ds_read_b64_tr_b16 v[214:215], v164 offset:41120
	ds_read_b64_tr_b16 v[218:219], v164 offset:41152
	ds_read_b64_tr_b16 v[222:223], v164 offset:41184
	ds_read_b64_tr_b16 v[200:201], v164 offset:42176
	ds_read_b64_tr_b16 v[216:217], v164 offset:42208
	ds_read_b64_tr_b16 v[220:221], v164 offset:42240
	ds_read_b64_tr_b16 v[224:225], v164 offset:42272
	v_mfma_f32_16x16x32_bf16 v[20:23], v[202:205], v[194:197], v[20:23]
	v_mfma_f32_16x16x32_bf16 v[16:19], v[206:209], v[194:197], v[16:19]
	ds_read_b128 v[202:205], v163 offset:64
	ds_read_b128 v[206:209], v163 offset:2624
	ds_read_b128 v[226:229], v163 offset:5184
	ds_read_b128 v[230:233], v163 offset:7744
	s_waitcnt lgkmcnt(12)
	v_mfma_f32_16x16x32_bf16 v[112:115], v[210:213], v[182:185], v[112:115]
	v_mfma_f32_16x16x32_bf16 v[80:83], v[210:213], v[186:189], v[80:83]
	v_mfma_f32_16x16x32_bf16 v[48:51], v[210:213], v[190:193], v[48:51]
	v_mfma_f32_16x16x32_bf16 v[12:15], v[210:213], v[194:197], v[12:15]
	s_waitcnt lgkmcnt(7)
	v_mfma_f32_16x16x32_bf16 v[108:111], v[198:201], v[182:185], v[108:111]
	s_waitcnt lgkmcnt(6)
	v_mfma_f32_16x16x32_bf16 v[104:107], v[214:217], v[182:185], v[104:107]
	s_waitcnt lgkmcnt(5)
	v_mfma_f32_16x16x32_bf16 v[100:103], v[218:221], v[182:185], v[100:103]
	s_waitcnt lgkmcnt(4)
	v_mfma_f32_16x16x32_bf16 v[96:99], v[222:225], v[182:185], v[96:99]
	v_mfma_f32_16x16x32_bf16 v[76:79], v[198:201], v[186:189], v[76:79]
	v_mfma_f32_16x16x32_bf16 v[72:75], v[214:217], v[186:189], v[72:75]
	v_mfma_f32_16x16x32_bf16 v[68:71], v[218:221], v[186:189], v[68:71]
	v_mfma_f32_16x16x32_bf16 v[64:67], v[222:225], v[186:189], v[64:67]
	v_mfma_f32_16x16x32_bf16 v[44:47], v[198:201], v[190:193], v[44:47]
	v_mfma_f32_16x16x32_bf16 v[40:43], v[214:217], v[190:193], v[40:43]
	v_mfma_f32_16x16x32_bf16 v[36:39], v[218:221], v[190:193], v[36:39]
	v_mfma_f32_16x16x32_bf16 v[32:35], v[222:225], v[190:193], v[32:35]
	v_mfma_f32_16x16x32_bf16 v[8:11], v[198:201], v[194:197], v[8:11]
	ds_read_b64_tr_b16 v[182:183], v164 offset:49664
	ds_read_b64_tr_b16 v[186:187], v164 offset:49696
	ds_read_b64_tr_b16 v[190:191], v164 offset:49728
	ds_read_b64_tr_b16 v[198:199], v164 offset:49760
	ds_read_b64_tr_b16 v[184:185], v164 offset:50752
	ds_read_b64_tr_b16 v[188:189], v164 offset:50784
	ds_read_b64_tr_b16 v[192:193], v164 offset:50816
	ds_read_b64_tr_b16 v[200:201], v164 offset:50848
	v_mfma_f32_16x16x32_bf16 v[4:7], v[214:217], v[194:197], v[4:7]
	v_mfma_f32_16x16x32_bf16 v[0:3], v[218:221], v[194:197], v[0:3]
	v_mfma_f32_16x16x32_bf16 v[28:31], v[222:225], v[194:197], v[28:31]
	s_waitcnt lgkmcnt(3)
	v_mfma_f32_16x16x32_bf16 v[124:127], v[182:185], v[202:205], v[124:127]
	s_waitcnt lgkmcnt(2)
	v_mfma_f32_16x16x32_bf16 v[120:123], v[186:189], v[202:205], v[120:123]
	v_mfma_f32_16x16x32_bf16 v[92:95], v[182:185], v[206:209], v[92:95]
	v_mfma_f32_16x16x32_bf16 v[88:91], v[186:189], v[206:209], v[88:91]
	v_mfma_f32_16x16x32_bf16 v[60:63], v[182:185], v[226:229], v[60:63]
	v_mfma_f32_16x16x32_bf16 v[56:59], v[186:189], v[226:229], v[56:59]
	v_mfma_f32_16x16x32_bf16 v[24:27], v[182:185], v[230:233], v[24:27]
	v_mfma_f32_16x16x32_bf16 v[20:23], v[186:189], v[230:233], v[20:23]
	ds_read_b64_tr_b16 v[182:183], v164 offset:49792
	ds_read_b64_tr_b16 v[186:187], v164 offset:49824
	ds_read_b64_tr_b16 v[194:195], v164 offset:49856
	ds_read_b64_tr_b16 v[210:211], v164 offset:49888
	ds_read_b64_tr_b16 v[184:185], v164 offset:50880
	ds_read_b64_tr_b16 v[188:189], v164 offset:50912
	ds_read_b64_tr_b16 v[196:197], v164 offset:50944
	ds_read_b64_tr_b16 v[212:213], v164 offset:50976
	s_waitcnt lgkmcnt(9)
	v_mfma_f32_16x16x32_bf16 v[116:119], v[190:193], v[202:205], v[116:119]
	s_waitcnt lgkmcnt(8)
	v_mfma_f32_16x16x32_bf16 v[112:115], v[198:201], v[202:205], v[112:115]
	v_mfma_f32_16x16x32_bf16 v[84:87], v[190:193], v[206:209], v[84:87]
	v_mfma_f32_16x16x32_bf16 v[80:83], v[198:201], v[206:209], v[80:83]
	v_mfma_f32_16x16x32_bf16 v[52:55], v[190:193], v[226:229], v[52:55]
	v_mfma_f32_16x16x32_bf16 v[48:51], v[198:201], v[226:229], v[48:51]
	v_mfma_f32_16x16x32_bf16 v[16:19], v[190:193], v[230:233], v[16:19]
	v_mfma_f32_16x16x32_bf16 v[12:15], v[198:201], v[230:233], v[12:15]
	s_waitcnt lgkmcnt(3)
	v_mfma_f32_16x16x32_bf16 v[108:111], v[182:185], v[202:205], v[108:111]
	s_waitcnt lgkmcnt(0)
	s_barrier
; template <bool UP>
; __device__ __forceinline__ void xgemm_unit(const Args& a, LAS unsigned char* lds, int e, int s, int cnt, int off_e, int rp, int tid, int lane, int wave) {
;     ...
;             __syncthreads();
; #pragma unroll 1
;             for (int t = 0; t < NK; t += 2) {
;                 XG_COMPUTE(0);
;                 __syncthreads();
;                 XG_COMPUTE(XG_BUF);
;                 __syncthreads();
;             }
	v_mfma_f32_16x16x32_bf16 v[104:107], v[186:189], v[202:205], v[104:107]
	v_mfma_f32_16x16x32_bf16 v[100:103], v[194:197], v[202:205], v[100:103]
	v_mfma_f32_16x16x32_bf16 v[96:99], v[210:213], v[202:205], v[96:99]
	v_mfma_f32_16x16x32_bf16 v[76:79], v[182:185], v[206:209], v[76:79]
	v_mfma_f32_16x16x32_bf16 v[72:75], v[186:189], v[206:209], v[72:75]
	v_mfma_f32_16x16x32_bf16 v[68:71], v[194:197], v[206:209], v[68:71]
	v_mfma_f32_16x16x32_bf16 v[64:67], v[210:213], v[206:209], v[64:67]
	v_mfma_f32_16x16x32_bf16 v[44:47], v[182:185], v[226:229], v[44:47]
	v_mfma_f32_16x16x32_bf16 v[40:43], v[186:189], v[226:229], v[40:43]
	v_mfma_f32_16x16x32_bf16 v[8:11], v[182:185], v[230:233], v[8:11]
	ds_read_b128 v[182:185], v163 offset:58368
	ds_read_b128 v[190:193], v163 offset:60928
	ds_read_b128 v[198:201], v163 offset:63488
	ds_read_b128 v[202:205], v165 offset:58368
	v_mfma_f32_16x16x32_bf16 v[4:7], v[186:189], v[230:233], v[4:7]
	ds_read_b64_tr_b16 v[186:187], v166
	ds_read_b64_tr_b16 v[206:207], v166 offset:32
	ds_read_b64_tr_b16 v[214:215], v166 offset:64
	ds_read_b64_tr_b16 v[218:219], v166 offset:96
	ds_read_b64_tr_b16 v[188:189], v166 offset:1088
	ds_read_b64_tr_b16 v[208:209], v166 offset:1120
	ds_read_b64_tr_b16 v[216:217], v166 offset:1152
	ds_read_b64_tr_b16 v[220:221], v166 offset:1184
	v_mfma_f32_16x16x32_bf16 v[36:39], v[194:197], v[226:229], v[36:39]
	v_mfma_f32_16x16x32_bf16 v[32:35], v[210:213], v[226:229], v[32:35]
	v_mfma_f32_16x16x32_bf16 v[0:3], v[194:197], v[230:233], v[0:3]
	v_mfma_f32_16x16x32_bf16 v[194:197], v[210:213], v[230:233], v[28:31]
	s_waitcnt lgkmcnt(3)
	v_mfma_f32_16x16x32_bf16 v[124:127], v[186:189], v[182:185], v[124:127]
	s_waitcnt lgkmcnt(2)
	v_mfma_f32_16x16x32_bf16 v[120:123], v[206:209], v[182:185], v[120:123]
	s_waitcnt lgkmcnt(1)
	v_mfma_f32_16x16x32_bf16 v[116:119], v[214:217], v[182:185], v[116:119]
	v_mfma_f32_16x16x32_bf16 v[92:95], v[186:189], v[190:193], v[92:95]
	v_mfma_f32_16x16x32_bf16 v[88:91], v[206:209], v[190:193], v[88:91]
	v_mfma_f32_16x16x32_bf16 v[84:87], v[214:217], v[190:193], v[84:87]
	v_mfma_f32_16x16x32_bf16 v[60:63], v[186:189], v[198:201], v[60:63]
	v_mfma_f32_16x16x32_bf16 v[56:59], v[206:209], v[198:201], v[56:59]
	v_mfma_f32_16x16x32_bf16 v[52:55], v[214:217], v[198:201], v[52:55]
	v_mfma_f32_16x16x32_bf16 v[24:27], v[186:189], v[202:205], v[24:27]
	ds_read_b64_tr_b16 v[186:187], v166 offset:128
	ds_read_b64_tr_b16 v[210:211], v166 offset:160
	ds_read_b64_tr_b16 v[222:223], v166 offset:192
	ds_read_b64_tr_b16 v[226:227], v166 offset:224
	ds_read_b64_tr_b16 v[188:189], v166 offset:1216
	ds_read_b64_tr_b16 v[212:213], v166 offset:1248
	ds_read_b64_tr_b16 v[224:225], v166 offset:1280
	ds_read_b64_tr_b16 v[228:229], v166 offset:1312
	v_mfma_f32_16x16x32_bf16 v[20:23], v[206:209], v[202:205], v[20:23]
	v_mfma_f32_16x16x32_bf16 v[16:19], v[214:217], v[202:205], v[16:19]
	ds_read_b128 v[206:209], v163 offset:58432
	ds_read_b128 v[214:217], v163 offset:60992
	ds_read_b128 v[230:233], v163 offset:63552
	ds_read_b128 v[28:31], v165 offset:58432
	s_waitcnt lgkmcnt(12)
	v_mfma_f32_16x16x32_bf16 v[112:115], v[218:221], v[182:185], v[112:115]
	v_mfma_f32_16x16x32_bf16 v[80:83], v[218:221], v[190:193], v[80:83]
	v_mfma_f32_16x16x32_bf16 v[48:51], v[218:221], v[198:201], v[48:51]
	v_mfma_f32_16x16x32_bf16 v[12:15], v[218:221], v[202:205], v[12:15]
	s_waitcnt lgkmcnt(7)
	v_mfma_f32_16x16x32_bf16 v[108:111], v[186:189], v[182:185], v[108:111]
	s_waitcnt lgkmcnt(6)
	v_mfma_f32_16x16x32_bf16 v[104:107], v[210:213], v[182:185], v[104:107]
	s_waitcnt lgkmcnt(5)
	v_mfma_f32_16x16x32_bf16 v[100:103], v[222:225], v[182:185], v[100:103]
	s_waitcnt lgkmcnt(4)
	v_mfma_f32_16x16x32_bf16 v[96:99], v[226:229], v[182:185], v[96:99]
	v_mfma_f32_16x16x32_bf16 v[76:79], v[186:189], v[190:193], v[76:79]
	v_mfma_f32_16x16x32_bf16 v[72:75], v[210:213], v[190:193], v[72:75]
	v_mfma_f32_16x16x32_bf16 v[68:71], v[222:225], v[190:193], v[68:71]
	v_mfma_f32_16x16x32_bf16 v[64:67], v[226:229], v[190:193], v[64:67]
	v_mfma_f32_16x16x32_bf16 v[44:47], v[186:189], v[198:201], v[44:47]
	v_mfma_f32_16x16x32_bf16 v[40:43], v[210:213], v[198:201], v[40:43]
	v_mfma_f32_16x16x32_bf16 v[36:39], v[222:225], v[198:201], v[36:39]
	v_mfma_f32_16x16x32_bf16 v[32:35], v[226:229], v[198:201], v[32:35]
	v_mfma_f32_16x16x32_bf16 v[8:11], v[186:189], v[202:205], v[8:11]
	ds_read_b64_tr_b16 v[182:183], v166 offset:8704
	ds_read_b64_tr_b16 v[186:187], v166 offset:8736
	ds_read_b64_tr_b16 v[190:191], v166 offset:8768
	ds_read_b64_tr_b16 v[198:199], v166 offset:8800
	ds_read_b64_tr_b16 v[184:185], v166 offset:9792
	ds_read_b64_tr_b16 v[188:189], v166 offset:9824
	ds_read_b64_tr_b16 v[192:193], v166 offset:9856
	ds_read_b64_tr_b16 v[200:201], v166 offset:9888
	v_mfma_f32_16x16x32_bf16 v[4:7], v[210:213], v[202:205], v[4:7]
	v_mfma_f32_16x16x32_bf16 v[0:3], v[222:225], v[202:205], v[0:3]
	v_mfma_f32_16x16x32_bf16 v[194:197], v[226:229], v[202:205], v[194:197]
	s_waitcnt lgkmcnt(3)
	v_mfma_f32_16x16x32_bf16 v[124:127], v[182:185], v[206:209], v[124:127]
	s_waitcnt lgkmcnt(2)
	v_mfma_f32_16x16x32_bf16 v[120:123], v[186:189], v[206:209], v[120:123]
	v_mfma_f32_16x16x32_bf16 v[92:95], v[182:185], v[214:217], v[92:95]
	v_mfma_f32_16x16x32_bf16 v[88:91], v[186:189], v[214:217], v[88:91]
	v_mfma_f32_16x16x32_bf16 v[60:63], v[182:185], v[230:233], v[60:63]
	v_mfma_f32_16x16x32_bf16 v[56:59], v[186:189], v[230:233], v[56:59]
	v_mfma_f32_16x16x32_bf16 v[24:27], v[182:185], v[28:31], v[24:27]
	v_mfma_f32_16x16x32_bf16 v[20:23], v[186:189], v[28:31], v[20:23]
	ds_read_b64_tr_b16 v[182:183], v166 offset:8832
	ds_read_b64_tr_b16 v[186:187], v166 offset:8864
	ds_read_b64_tr_b16 v[202:203], v166 offset:8896
	ds_read_b64_tr_b16 v[210:211], v166 offset:8928
	ds_read_b64_tr_b16 v[184:185], v166 offset:9920
	ds_read_b64_tr_b16 v[188:189], v166 offset:9952
	ds_read_b64_tr_b16 v[204:205], v166 offset:9984
	ds_read_b64_tr_b16 v[212:213], v166 offset:10016
	s_waitcnt lgkmcnt(9)
	v_mfma_f32_16x16x32_bf16 v[116:119], v[190:193], v[206:209], v[116:119]
	s_waitcnt lgkmcnt(8)
	v_mfma_f32_16x16x32_bf16 v[112:115], v[198:201], v[206:209], v[112:115]
	v_mfma_f32_16x16x32_bf16 v[84:87], v[190:193], v[214:217], v[84:87]
	v_mfma_f32_16x16x32_bf16 v[80:83], v[198:201], v[214:217], v[80:83]
	v_mfma_f32_16x16x32_bf16 v[52:55], v[190:193], v[230:233], v[52:55]
	v_mfma_f32_16x16x32_bf16 v[48:51], v[198:201], v[230:233], v[48:51]
	v_mfma_f32_16x16x32_bf16 v[16:19], v[190:193], v[28:31], v[16:19]
	v_mfma_f32_16x16x32_bf16 v[12:15], v[198:201], v[28:31], v[12:15]
	s_waitcnt lgkmcnt(3)
	v_mfma_f32_16x16x32_bf16 v[108:111], v[182:185], v[206:209], v[108:111]
	s_add_i32 s0, s0, 2
	s_cmp_gt_u32 s0, 5
	s_waitcnt lgkmcnt(0)
	v_mfma_f32_16x16x32_bf16 v[104:107], v[186:189], v[206:209], v[104:107]
	s_barrier
; #define LAS __attribute__((address_space(3)))
; __device__ __forceinline__ unsigned pk2(float lo, float hi) { f32x2_t v = {lo, hi}; bf16x2_t b = __builtin_convertvector(v, bf16x2_t); return __builtin_bit_cast(unsigned, b); }
; __device__ __forceinline__ float swap1(float x) { return __int_as_float(__builtin_amdgcn_update_dpp(0, __float_as_int(x), 0xB1, 0xF, 0xF, true)); }
; template <bool UP>
; __device__ __forceinline__ void xgemm_unit(const Args& a, LAS unsigned char* lds, int e, int s, int cnt, int off_e, int rp, int tid, int lane, int wave) {
;     ...
;             __syncthreads();
; #pragma unroll 1
;             for (int t = 0; t < NK; t += 2) {
;                 XG_COMPUTE(0);
;                 __syncthreads();
;                 XG_COMPUTE(XG_BUF);
;                 __syncthreads();
;             }
;     ...
;                 } else {
;                     LAS unsigned char* stg = lds + XG_BUF + cw * 8704;
; #pragma unroll
;                     for (int h = 0; h < 2; ++h) {
; #pragma unroll
;                         for (int m2 = 0; m2 < 2; ++m2)
; #pragma unroll
;                             for (int r = 0; r < 4; ++r) { const int mi = 2 * h + m2, lrow = 16 * m2 + 4 * g + r; const float w = __int_as_float(rinfo[2 * (16 * mi + 4 * g + r) + 1]);
; #pragma unroll
;                                 for (int q = 0; q < 4; ++q) { const float a0 = acc[mi][2 * q][r] * w, a1 = acc[mi][2 * q + 1][r] * w;
;                                     const float got = swap1(odd ? a0 : a1);
;                                     const unsigned pk = odd ? pk2(got, a1) : pk2(a0, got);
;                                     const int col = odd ? (16 * (2 * q + 1) + i - 1) : (16 * (2 * q) + i);
;                                     *(LAS unsigned*)(stg + lrow * 272 + col * 2) = pk; } }
; #pragma unroll 2
;                         for (int jj = 0; jj < 8; ++jj) { const int lrow = (lane >> 4) + 4 * jj, c = lane & 15, row = 64 * cw + 32 * h + lrow;
;                             const v4u o = *(const LAS v4u*)(stg + lrow * 272 + 16 * c);
;                             if (row < nrows) { const int as = rinfo[2 * (32 * h + lrow)]; *(v4u*)(YA + (size_t)as * D + 128 * s + 8 * c) = o; } }
;                     }
	v_mfma_f32_16x16x32_bf16 v[100:103], v[202:205], v[206:209], v[100:103]
	v_mfma_f32_16x16x32_bf16 v[96:99], v[210:213], v[206:209], v[96:99]
	v_mfma_f32_16x16x32_bf16 v[76:79], v[182:185], v[214:217], v[76:79]
	v_mfma_f32_16x16x32_bf16 v[72:75], v[186:189], v[214:217], v[72:75]
	v_mfma_f32_16x16x32_bf16 v[68:71], v[202:205], v[214:217], v[68:71]
	v_mfma_f32_16x16x32_bf16 v[64:67], v[210:213], v[214:217], v[64:67]
	v_mfma_f32_16x16x32_bf16 v[44:47], v[182:185], v[230:233], v[44:47]
	v_mfma_f32_16x16x32_bf16 v[40:43], v[186:189], v[230:233], v[40:43]
	v_mfma_f32_16x16x32_bf16 v[36:39], v[202:205], v[230:233], v[36:39]
	v_mfma_f32_16x16x32_bf16 v[32:35], v[210:213], v[230:233], v[32:35]
	v_mfma_f32_16x16x32_bf16 v[8:11], v[182:185], v[28:31], v[8:11]
	v_mfma_f32_16x16x32_bf16 v[4:7], v[186:189], v[28:31], v[4:7]
	v_mfma_f32_16x16x32_bf16 v[0:3], v[202:205], v[28:31], v[0:3]
	v_mfma_f32_16x16x32_bf16 v[28:31], v[210:213], v[28:31], v[194:197]
	s_cbranch_scc0 .LBB0_1266
	s_nop 7
	s_nop 7
	v_and_b32_e32 v182, 15, v175
	v_lshl_add_u32 v183, v182, 3, s23
	ds_read_b64 v[184:185], v183
	ds_read_b64 v[186:187], v183 offset:128
	ds_read_b64 v[188:189], v183 offset:256
	ds_read_b64 v[190:191], v183 offset:384
	v_lshrrev_b32_e32 v192, 4, v175
	v_and_b32_e32 v193, 1, v192
	v_lshlrev_b32_e32 v192, 3, v192
	v_mad_u32_u24 v192, v193, 24, v192
	s_lshl_b32 s0, s83, 8
	s_add_u32 s0, s58, s0
	s_addc_u32 s1, s59, 0
	s_add_u32 s0, s0, 0x18800000
	s_addc_u32 s1, s1, 0
	v_mov_b32_e32 v193, 0
	v_lshl_add_u64 v[194:195], s[0:1], 0, v[192:193]
	v_and_b32_e32 v196, 0xc0, v162
	v_or_b32_e32 v196, v196, v182
	v_mov_b32_e32 v199, 0
	s_waitcnt lgkmcnt(3)
	v_mov_b32_e32 v202, v185
	v_mov_b32_e32 v203, v185
	v_lshlrev_b32_e32 v198, 12, v184
	v_lshl_add_u64 v[200:201], v[194:195], 0, v[198:199]
	v_mov_b32_e32 v197, v196
	v_pk_mul_f32 v[124:125], v[124:125], v[202:203]
	v_pk_mul_f32 v[126:127], v[126:127], v[202:203]
	v_pk_mul_f32 v[120:121], v[120:121], v[202:203]
	v_pk_mul_f32 v[122:123], v[122:123], v[202:203]
	v_cvt_pk_bf16_f32 v204, v124, v125
	v_cvt_pk_bf16_f32 v205, v126, v127
	v_cvt_pk_bf16_f32 v206, v120, v121
	v_cvt_pk_bf16_f32 v207, v122, v123
	v_pk_mul_f32 v[116:117], v[116:117], v[202:203]
	v_pk_mul_f32 v[118:119], v[118:119], v[202:203]
	v_pk_mul_f32 v[112:113], v[112:113], v[202:203]
	v_pk_mul_f32 v[114:115], v[114:115], v[202:203]
	v_cvt_pk_bf16_f32 v208, v116, v117
	v_cvt_pk_bf16_f32 v209, v118, v119
	v_cvt_pk_bf16_f32 v210, v112, v113
	v_cvt_pk_bf16_f32 v211, v114, v115
	v_pk_mul_f32 v[108:109], v[108:109], v[202:203]
	v_pk_mul_f32 v[110:111], v[110:111], v[202:203]
	v_pk_mul_f32 v[104:105], v[104:105], v[202:203]
	v_pk_mul_f32 v[106:107], v[106:107], v[202:203]
	v_cvt_pk_bf16_f32 v212, v108, v109
	v_cvt_pk_bf16_f32 v213, v110, v111
	v_cvt_pk_bf16_f32 v214, v104, v105
	v_cvt_pk_bf16_f32 v215, v106, v107
	v_pk_mul_f32 v[100:101], v[100:101], v[202:203]
	v_pk_mul_f32 v[102:103], v[102:103], v[202:203]
	v_pk_mul_f32 v[96:97], v[96:97], v[202:203]
	v_pk_mul_f32 v[98:99], v[98:99], v[202:203]
	v_cvt_pk_bf16_f32 v216, v100, v101
	v_cvt_pk_bf16_f32 v217, v102, v103
	v_cvt_pk_bf16_f32 v218, v96, v97
	v_cvt_pk_bf16_f32 v219, v98, v99
	s_nop 1
	v_permlane16_swap_b32_e32 v204, v206
	v_permlane16_swap_b32_e32 v205, v207
	v_permlane16_swap_b32_e32 v208, v210
	v_permlane16_swap_b32_e32 v209, v211
	v_permlane16_swap_b32_e32 v212, v214
	v_permlane16_swap_b32_e32 v213, v215
	v_permlane16_swap_b32_e32 v216, v218
	v_permlane16_swap_b32_e32 v217, v219
	v_cmp_gt_i32_e32 vcc, s86, v197
	s_and_saveexec_b64 s[0:1], vcc
	global_store_dwordx4 v[200:201], v[204:207], off
	global_store_dwordx4 v[200:201], v[208:211], off offset:64
	global_store_dwordx4 v[200:201], v[212:215], off offset:128
	global_store_dwordx4 v[200:201], v[216:219], off offset:192
	s_or_b64 exec, exec, s[0:1]
	s_waitcnt lgkmcnt(2)
	v_mov_b32_e32 v202, v187
	v_mov_b32_e32 v203, v187
	v_lshlrev_b32_e32 v198, 12, v186
	v_lshl_add_u64 v[200:201], v[194:195], 0, v[198:199]
	v_add_u32_e32 v197, 16, v196
	v_pk_mul_f32 v[92:93], v[92:93], v[202:203]
	v_pk_mul_f32 v[94:95], v[94:95], v[202:203]
	v_pk_mul_f32 v[88:89], v[88:89], v[202:203]
	v_pk_mul_f32 v[90:91], v[90:91], v[202:203]
	v_cvt_pk_bf16_f32 v204, v92, v93
	v_cvt_pk_bf16_f32 v205, v94, v95
	v_cvt_pk_bf16_f32 v206, v88, v89
	v_cvt_pk_bf16_f32 v207, v90, v91
	v_pk_mul_f32 v[84:85], v[84:85], v[202:203]
	v_pk_mul_f32 v[86:87], v[86:87], v[202:203]
	v_pk_mul_f32 v[80:81], v[80:81], v[202:203]
	v_pk_mul_f32 v[82:83], v[82:83], v[202:203]
	v_cvt_pk_bf16_f32 v208, v84, v85
	v_cvt_pk_bf16_f32 v209, v86, v87
	v_cvt_pk_bf16_f32 v210, v80, v81
	v_cvt_pk_bf16_f32 v211, v82, v83
	v_pk_mul_f32 v[76:77], v[76:77], v[202:203]
	v_pk_mul_f32 v[78:79], v[78:79], v[202:203]
	v_pk_mul_f32 v[72:73], v[72:73], v[202:203]
	v_pk_mul_f32 v[74:75], v[74:75], v[202:203]
	v_cvt_pk_bf16_f32 v212, v76, v77
	v_cvt_pk_bf16_f32 v213, v78, v79
	v_cvt_pk_bf16_f32 v214, v72, v73
	v_cvt_pk_bf16_f32 v215, v74, v75
	v_pk_mul_f32 v[68:69], v[68:69], v[202:203]
	v_pk_mul_f32 v[70:71], v[70:71], v[202:203]
	v_pk_mul_f32 v[64:65], v[64:65], v[202:203]
	v_pk_mul_f32 v[66:67], v[66:67], v[202:203]
	v_cvt_pk_bf16_f32 v216, v68, v69
	v_cvt_pk_bf16_f32 v217, v70, v71
	v_cvt_pk_bf16_f32 v218, v64, v65
	v_cvt_pk_bf16_f32 v219, v66, v67
	s_nop 1
	v_permlane16_swap_b32_e32 v204, v206
	v_permlane16_swap_b32_e32 v205, v207
	v_permlane16_swap_b32_e32 v208, v210
	v_permlane16_swap_b32_e32 v209, v211
	v_permlane16_swap_b32_e32 v212, v214
	v_permlane16_swap_b32_e32 v213, v215
	v_permlane16_swap_b32_e32 v216, v218
	v_permlane16_swap_b32_e32 v217, v219
	v_cmp_gt_i32_e32 vcc, s86, v197
	s_and_saveexec_b64 s[0:1], vcc
	global_store_dwordx4 v[200:201], v[204:207], off
	global_store_dwordx4 v[200:201], v[208:211], off offset:64
	global_store_dwordx4 v[200:201], v[212:215], off offset:128
	global_store_dwordx4 v[200:201], v[216:219], off offset:192
	s_or_b64 exec, exec, s[0:1]
	s_waitcnt lgkmcnt(1)
; #define LAS __attribute__((address_space(3)))
; template <bool UP>
; __device__ __forceinline__ void xgemm_unit(const Args& a, LAS unsigned char* lds, int e, int s, int cnt, int off_e, int rp, int tid, int lane, int wave) {
;     ...
;         const int nrows = (cnt - rp < XG_RM) ? (cnt - rp) : XG_RM;
;         if (loader) {
;             const int tl = tid & 255;
;             const int arow = tl >> 3, ach = tl & 7;
;             const int n4 = UP ? (tl & 15) : (tl & 31), kr = UP ? ((tl >> 4) & 7) : (tl >> 5), bcol = UP ? (64 * ((wave >> 1) & 1) + 4 * n4) : 4 * n4;
;             const float* Bu = UP ? ((((wave >> 1) & 1) ? a.in[I_W3] : a.in[I_W1]) + (size_t)e * D * DE) : (a.in[I_W2] + (size_t)e * DE * D);
;             const __amdgpu_buffer_rsrc_t rB = __builtin_amdgcn_make_buffer_rsrc((void*)Bu, (short)0, K * LDB * 4, 0x00020000);
;             const __amdgpu_buffer_rsrc_t rA = __builtin_amdgcn_make_buffer_rsrc((void*)Abase, (short)0, UP ? T * D * 2 : 2 * T * DE * 2, 0x00020000);
;     ...
;                 } else {
;                     LAS unsigned char* stg = lds + XG_BUF + cw * 8704;
; #pragma unroll
;                     for (int h = 0; h < 2; ++h) {
; #pragma unroll
;                         for (int m2 = 0; m2 < 2; ++m2)
; #pragma unroll
;                             for (int r = 0; r < 4; ++r) { const int mi = 2 * h + m2, lrow = 16 * m2 + 4 * g + r; const float w = __int_as_float(rinfo[2 * (16 * mi + 4 * g + r) + 1]);
; #pragma unroll
;                                 for (int q = 0; q < 4; ++q) { const float a0 = acc[mi][2 * q][r] * w, a1 = acc[mi][2 * q + 1][r] * w;
;                                     const float got = swap1(odd ? a0 : a1);
;                                     const unsigned pk = odd ? pk2(got, a1) : pk2(a0, got);
;                                     const int col = odd ? (16 * (2 * q + 1) + i - 1) : (16 * (2 * q) + i);
;                                     *(LAS unsigned*)(stg + lrow * 272 + col * 2) = pk; } }
; #pragma unroll 2
;                         for (int jj = 0; jj < 8; ++jj) { const int lrow = (lane >> 4) + 4 * jj, c = lane & 15, row = 64 * cw + 32 * h + lrow;
;                             const v4u o = *(const LAS v4u*)(stg + lrow * 272 + 16 * c);
;                             if (row < nrows) { const int as = rinfo[2 * (32 * h + lrow)]; *(v4u*)(YA + (size_t)as * D + 128 * s + 8 * c) = o; } }
;                     }
	v_mov_b32_e32 v202, v189
	v_mov_b32_e32 v203, v189
	v_lshlrev_b32_e32 v198, 12, v188
	v_lshl_add_u64 v[200:201], v[194:195], 0, v[198:199]
	v_add_u32_e32 v197, 32, v196
	v_pk_mul_f32 v[60:61], v[60:61], v[202:203]
	v_pk_mul_f32 v[62:63], v[62:63], v[202:203]
	v_pk_mul_f32 v[56:57], v[56:57], v[202:203]
	v_pk_mul_f32 v[58:59], v[58:59], v[202:203]
	v_cvt_pk_bf16_f32 v204, v60, v61
	v_cvt_pk_bf16_f32 v205, v62, v63
	v_cvt_pk_bf16_f32 v206, v56, v57
	v_cvt_pk_bf16_f32 v207, v58, v59
	v_pk_mul_f32 v[52:53], v[52:53], v[202:203]
	v_pk_mul_f32 v[54:55], v[54:55], v[202:203]
	v_pk_mul_f32 v[48:49], v[48:49], v[202:203]
	v_pk_mul_f32 v[50:51], v[50:51], v[202:203]
	v_cvt_pk_bf16_f32 v208, v52, v53
	v_cvt_pk_bf16_f32 v209, v54, v55
	v_cvt_pk_bf16_f32 v210, v48, v49
	v_cvt_pk_bf16_f32 v211, v50, v51
	v_pk_mul_f32 v[44:45], v[44:45], v[202:203]
	v_pk_mul_f32 v[46:47], v[46:47], v[202:203]
	v_pk_mul_f32 v[40:41], v[40:41], v[202:203]
	v_pk_mul_f32 v[42:43], v[42:43], v[202:203]
	v_cvt_pk_bf16_f32 v212, v44, v45
	v_cvt_pk_bf16_f32 v213, v46, v47
	v_cvt_pk_bf16_f32 v214, v40, v41
	v_cvt_pk_bf16_f32 v215, v42, v43
	v_pk_mul_f32 v[36:37], v[36:37], v[202:203]
	v_pk_mul_f32 v[38:39], v[38:39], v[202:203]
	v_pk_mul_f32 v[32:33], v[32:33], v[202:203]
	v_pk_mul_f32 v[34:35], v[34:35], v[202:203]
	v_cvt_pk_bf16_f32 v216, v36, v37
	v_cvt_pk_bf16_f32 v217, v38, v39
	v_cvt_pk_bf16_f32 v218, v32, v33
	v_cvt_pk_bf16_f32 v219, v34, v35
	s_nop 1
	v_permlane16_swap_b32_e32 v204, v206
	v_permlane16_swap_b32_e32 v205, v207
	v_permlane16_swap_b32_e32 v208, v210
	v_permlane16_swap_b32_e32 v209, v211
	v_permlane16_swap_b32_e32 v212, v214
	v_permlane16_swap_b32_e32 v213, v215
	v_permlane16_swap_b32_e32 v216, v218
	v_permlane16_swap_b32_e32 v217, v219
	v_cmp_gt_i32_e32 vcc, s86, v197
	s_and_saveexec_b64 s[0:1], vcc
	global_store_dwordx4 v[200:201], v[204:207], off
	global_store_dwordx4 v[200:201], v[208:211], off offset:64
	global_store_dwordx4 v[200:201], v[212:215], off offset:128
	global_store_dwordx4 v[200:201], v[216:219], off offset:192
	s_or_b64 exec, exec, s[0:1]
	s_waitcnt lgkmcnt(0)
	v_mov_b32_e32 v202, v191
	v_mov_b32_e32 v203, v191
	v_lshlrev_b32_e32 v198, 12, v190
	v_lshl_add_u64 v[200:201], v[194:195], 0, v[198:199]
	v_add_u32_e32 v197, 48, v196
	v_pk_mul_f32 v[24:25], v[24:25], v[202:203]
	v_pk_mul_f32 v[26:27], v[26:27], v[202:203]
	v_pk_mul_f32 v[20:21], v[20:21], v[202:203]
	v_pk_mul_f32 v[22:23], v[22:23], v[202:203]
	v_cvt_pk_bf16_f32 v204, v24, v25
	v_cvt_pk_bf16_f32 v205, v26, v27
	v_cvt_pk_bf16_f32 v206, v20, v21
	v_cvt_pk_bf16_f32 v207, v22, v23
	v_pk_mul_f32 v[16:17], v[16:17], v[202:203]
	v_pk_mul_f32 v[18:19], v[18:19], v[202:203]
	v_pk_mul_f32 v[12:13], v[12:13], v[202:203]
	v_pk_mul_f32 v[14:15], v[14:15], v[202:203]
	v_cvt_pk_bf16_f32 v208, v16, v17
	v_cvt_pk_bf16_f32 v209, v18, v19
	v_cvt_pk_bf16_f32 v210, v12, v13
	v_cvt_pk_bf16_f32 v211, v14, v15
	v_pk_mul_f32 v[8:9], v[8:9], v[202:203]
	v_pk_mul_f32 v[10:11], v[10:11], v[202:203]
	v_pk_mul_f32 v[4:5], v[4:5], v[202:203]
	v_pk_mul_f32 v[6:7], v[6:7], v[202:203]
	v_cvt_pk_bf16_f32 v212, v8, v9
	v_cvt_pk_bf16_f32 v213, v10, v11
	v_cvt_pk_bf16_f32 v214, v4, v5
	v_cvt_pk_bf16_f32 v215, v6, v7
	v_pk_mul_f32 v[0:1], v[0:1], v[202:203]
	v_pk_mul_f32 v[2:3], v[2:3], v[202:203]
	v_pk_mul_f32 v[28:29], v[28:29], v[202:203]
	v_pk_mul_f32 v[30:31], v[30:31], v[202:203]
	v_cvt_pk_bf16_f32 v216, v0, v1
	v_cvt_pk_bf16_f32 v217, v2, v3
	v_cvt_pk_bf16_f32 v218, v28, v29
	v_cvt_pk_bf16_f32 v219, v30, v31
	s_nop 1
	v_permlane16_swap_b32_e32 v204, v206
	v_permlane16_swap_b32_e32 v205, v207
	v_permlane16_swap_b32_e32 v208, v210
	v_permlane16_swap_b32_e32 v209, v211
	v_permlane16_swap_b32_e32 v212, v214
	v_permlane16_swap_b32_e32 v213, v215
	v_permlane16_swap_b32_e32 v216, v218
	v_permlane16_swap_b32_e32 v217, v219
	v_cmp_gt_i32_e32 vcc, s86, v197
	s_and_saveexec_b64 s[0:1], vcc
	global_store_dwordx4 v[200:201], v[204:207], off
	global_store_dwordx4 v[200:201], v[208:211], off offset:64
	global_store_dwordx4 v[200:201], v[212:215], off offset:128
	global_store_dwordx4 v[200:201], v[216:219], off offset:192
	s_or_b64 exec, exec, s[0:1]
	s_branch .LBB0_1263
.LBB0_1273:
	s_and_b64 vcc, exec, s[0:1]
	s_cbranch_vccz .LBB0_1263
	s_branch .LBB0_1281
.LBB0_1280:
	s_branch .LBB0_1263
.LBB0_1281:
	s_cmp_lg_u32 s100, 0
	s_cbranch_scc0 .Lxd_pro
	s_mov_b32 s12, s98
	s_mov_b32 s13, s99
	s_setprio 1
	s_branch .Lxd_body
; #define XG_ISSUE_B(pb_, t_) do { _Pragma("unroll") for (int j_ = 0; j_ < 8; ++j_) pb_[j_] = __builtin_bit_cast(f32x4, __builtin_amdgcn_raw_buffer_load_b128(rB, boff, (64 * (t_) + 8 * j_) * LDB * 4, 0)); } while (0)
; #define XG_ISSUE_A(pa_, t_) do { _Pragma("unroll") for (int j_ = 0; j_ < 8; ++j_) pa_[j_] = __builtin_amdgcn_raw_buffer_load_b128(rA, aoff[j_], 128 * (t_), 0); } while (0)
; template <bool UP>
; __device__ __forceinline__ void xgemm_unit(const Args& a, LAS unsigned char* lds, int e, int s, int cnt, int off_e, int rp, int tid, int lane, int wave) {
;     ...
;         const int nrows = (cnt - rp < XG_RM) ? (cnt - rp) : XG_RM;
;         if (loader) {
;             const int tl = tid & 255;
;             const int arow = tl >> 3, ach = tl & 7;
;             const int n4 = UP ? (tl & 15) : (tl & 31), kr = UP ? ((tl >> 4) & 7) : (tl >> 5), bcol = UP ? (64 * ((wave >> 1) & 1) + 4 * n4) : 4 * n4;
;             const float* Bu = UP ? ((((wave >> 1) & 1) ? a.in[I_W3] : a.in[I_W1]) + (size_t)e * D * DE) : (a.in[I_W2] + (size_t)e * DE * D);
;             const __amdgpu_buffer_rsrc_t rB = __builtin_amdgcn_make_buffer_rsrc((void*)Bu, (short)0, K * LDB * 4, 0x00020000);
;             const __amdgpu_buffer_rsrc_t rA = __builtin_amdgcn_make_buffer_rsrc((void*)Abase, (short)0, UP ? T * D * 2 : 2 * T * DE * 2, 0x00020000);
;             const unsigned boff = (unsigned)(kr * LDB + 4 * n4 + (UP ? 64 : 128) * s) * 4u;
;             const int bdst = XG_ABYTES + kr * XG_BP + bcol * 2;
;             unsigned aoff[8];
; #pragma unroll
;             for (int j = 0; j < 8; ++j) { int rr = arow + 32 * j; rr = (rr < nrows) ? rr : (nrows - 1);
;                 if (UP) aoff[j] = ((unsigned)(LISTS[rp + rr] >> 1) * (unsigned)D + ach * 8) * 2u; else aoff[j] = ((unsigned)(off_e + rp + rr) * (unsigned)DE + ach * 8) * 2u; }
;             f32x4 pb0[8], pb1[8], pb2[8]; v4u pa0[8], pa1[8], pa2[8];
;             static_assert(NK % 3 == 2, "loader ring schedule");
;     ...
;             __builtin_amdgcn_s_setprio(1);
;             int ras_ = 0; float rw_ = 0.f;
;             if (!UP) ras_ = LISTS[rp + ((tl < nrows) ? tl : nrows - 1)];
;             XG_ISSUE_A(pa0, 0); XG_ISSUE_B(pb0, 0); XG_ISSUE_A(pa1, 1); XG_ISSUE_B(pb1, 1); XG_ISSUE_B(pb2, 2);
.Lxd_pro:
	s_lshl_b32 s0, s12, 15
	s_add_u32 s0, s25, s0
	s_addc_u32 s1, s26, 0
	s_lshl_b32 s12, s12, 22
	s_add_u32 s12, s54, s12
	s_addc_u32 s13, s55, 0
	s_add_i32 s20, s86, -1
	s_add_i32 s85, s85, s82
	v_min_i32_e32 v0, s20, v144
	v_add_u32_e32 v0, s85, v0
	v_lshl_or_b32 v2, v0, 10, v145
	v_min_i32_e32 v0, s20, v146
	v_add_u32_e32 v0, s85, v0
	v_lshl_or_b32 v3, v0, 10, v145
	v_min_i32_e32 v0, s20, v147
	v_add_u32_e32 v0, s85, v0
	v_lshl_or_b32 v4, v0, 10, v145
	v_min_i32_e32 v0, s20, v148
	v_add_u32_e32 v0, s85, v0
	v_lshl_or_b32 v5, v0, 10, v145
	v_min_i32_e32 v0, s20, v149
	v_add_u32_e32 v0, s85, v0
	v_lshl_or_b32 v6, v0, 10, v145
	v_min_i32_e32 v0, s20, v150
	v_add_u32_e32 v0, s85, v0
	v_lshl_or_b32 v7, v0, 10, v145
	v_min_i32_e32 v0, s20, v151
	v_add_u32_e32 v0, s85, v0
	v_lshl_or_b32 v8, v0, 10, v145
	v_min_i32_e32 v0, s20, v152
	v_add_u32_e32 v0, s85, v0
	s_and_b32 s13, s13, 0xffff
	v_lshl_or_b32 v9, v0, 10, v145
	s_setprio 1
	v_lshl_or_b32 v181, s83, 9, v174
	s_mov_b32 s83, 0x10000
	buffer_load_dwordx4 v[10:13], v181, s[12:15], 0 offen
	buffer_load_dwordx4 v[14:17], v181, s[12:15], s83 offen
	buffer_load_dwordx4 v[18:21], v181, s[12:15], s15 offen
	s_mov_b32 s83, 0x30000
	v_mov_b32_e32 v0, s20
	v_cmp_gt_i32_e32 vcc, s84, v143
	buffer_load_dwordx4 v[22:25], v181, s[12:15], s83 offen
	s_mov_b32 s83, 0x40000
	v_cndmask_b32_e32 v0, v0, v143, vcc
	buffer_load_dwordx4 v[26:29], v181, s[12:15], s83 offen
	s_mov_b32 s83, 0x50000
	v_add_u32_e32 v0, s82, v0
	buffer_load_dwordx4 v[30:33], v181, s[12:15], s83 offen
	s_mov_b32 s83, 0x60000
	v_ashrrev_i32_e32 v1, 31, v0
	buffer_load_dwordx4 v[34:37], v181, s[12:15], s83 offen
	s_mov_b32 s83, 0x70000
	v_lshl_add_u64 v[0:1], v[0:1], 2, s[0:1]
	s_mov_b32 s0, 0x80000
	buffer_load_dwordx4 v[38:41], v181, s[12:15], s83 offen
	buffer_load_dwordx4 v[42:45], v2, s[8:11], 0 offen
	buffer_load_dwordx4 v[46:49], v3, s[8:11], 0 offen
	buffer_load_dwordx4 v[50:53], v4, s[8:11], 0 offen
	buffer_load_dwordx4 v[54:57], v5, s[8:11], 0 offen
	buffer_load_dwordx4 v[58:61], v6, s[8:11], 0 offen
	buffer_load_dwordx4 v[62:65], v7, s[8:11], 0 offen
	buffer_load_dwordx4 v[66:69], v8, s[8:11], 0 offen
	buffer_load_dwordx4 v[70:73], v9, s[8:11], 0 offen
	buffer_load_dwordx4 v[74:77], v181, s[12:15], s0 offen
	s_mov_b32 s0, 0x90000
	buffer_load_dwordx4 v[78:81], v181, s[12:15], s0 offen
	s_mov_b32 s0, 0xa0000
	global_load_dword v228, v[0:1], off
	s_nop 0
	buffer_load_dwordx4 v[82:85], v181, s[12:15], s0 offen
	buffer_load_dwordx4 v[86:89], v2, s[8:11], s24 offen
	buffer_load_dwordx4 v[90:93], v3, s[8:11], s24 offen
	s_mov_b32 s0, 0xb0000
	buffer_load_dwordx4 v[94:97], v181, s[12:15], s0 offen
	buffer_load_dwordx4 v[98:101], v4, s[8:11], s24 offen
	buffer_load_dwordx4 v[102:105], v5, s[8:11], s24 offen
	s_mov_b32 s0, 0xc0000
	buffer_load_dwordx4 v[106:109], v181, s[12:15], s0 offen
	buffer_load_dwordx4 v[110:113], v6, s[8:11], s24 offen
	buffer_load_dwordx4 v[114:117], v7, s[8:11], s24 offen
	s_mov_b32 s0, 0xd0000
	buffer_load_dwordx4 v[118:121], v181, s[12:15], s0 offen
	buffer_load_dwordx4 v[122:125], v8, s[8:11], s24 offen
	buffer_load_dwordx4 v[182:185], v9, s[8:11], s24 offen
	s_mov_b32 s0, 0xe0000
	buffer_load_dwordx4 v[186:189], v181, s[12:15], s0 offen
	s_mov_b32 s0, 0xf0000
	buffer_load_dwordx4 v[190:193], v181, s[12:15], s0 offen
	s_mov_b32 s0, 0x100000
	buffer_load_dwordx4 v[194:197], v181, s[12:15], s0 offen
	s_mov_b32 s0, 0x110000
	buffer_load_dwordx4 v[198:201], v181, s[12:15], s0 offen
	s_mov_b32 s0, 0x120000
	buffer_load_dwordx4 v[202:205], v181, s[12:15], s0 offen
	s_mov_b32 s0, 0x130000
	buffer_load_dwordx4 v[206:209], v181, s[12:15], s0 offen
	s_mov_b32 s0, 0x140000
	buffer_load_dwordx4 v[210:213], v181, s[12:15], s0 offen
	s_mov_b32 s0, 0x150000
	buffer_load_dwordx4 v[214:217], v181, s[12:15], s0 offen
	buffer_load_dwordx4 v[218:221], v181, s[12:15], s28 offen
	buffer_load_dwordx4 v[222:225], v181, s[12:15], s29 offen
.Lxd_body:
	s_add_i32 s0, 0, 0xe400
	s_waitcnt vmcnt(40)
	v_cvt_pk_bf16_f32 v10, v10, v11
	v_cvt_pk_bf16_f32 v11, v12, v13
	s_waitcnt vmcnt(39)
	v_cvt_pk_bf16_f32 v12, v14, v15
	v_cvt_pk_bf16_f32 v13, v16, v17
	s_waitcnt vmcnt(38)
	v_cvt_pk_bf16_f32 v14, v18, v19
	v_cvt_pk_bf16_f32 v15, v20, v21
	s_waitcnt vmcnt(37)
	v_cvt_pk_bf16_f32 v16, v22, v23
	v_cvt_pk_bf16_f32 v17, v24, v25
	s_waitcnt vmcnt(36)
	v_cvt_pk_bf16_f32 v18, v26, v27
	v_cvt_pk_bf16_f32 v19, v28, v29
	s_waitcnt vmcnt(35)
	v_cvt_pk_bf16_f32 v20, v30, v31
	v_cvt_pk_bf16_f32 v21, v32, v33
	s_waitcnt vmcnt(34)
	v_cvt_pk_bf16_f32 v22, v34, v35
	v_cvt_pk_bf16_f32 v23, v36, v37
	s_waitcnt vmcnt(33)
	v_cvt_pk_bf16_f32 v24, v38, v39
	v_cvt_pk_bf16_f32 v25, v40, v41
	ds_write_b64 v154, v[10:11] offset:40960
	ds_write_b64 v154, v[12:13] offset:43136
	ds_write_b64 v154, v[14:15] offset:45312
	ds_write_b64 v154, v[16:17] offset:47488
	ds_write_b64 v154, v[18:19] offset:49664
	ds_write_b64 v154, v[20:21] offset:51840
	ds_write_b64 v154, v[22:23] offset:54016
	ds_write_b64 v154, v[24:25] offset:56192
	s_waitcnt vmcnt(32)
	ds_write_b128 v176, v[42:45]
	s_waitcnt vmcnt(31)
	ds_write_b128 v176, v[46:49] offset:5120
	s_waitcnt vmcnt(30)
	ds_write_b128 v176, v[50:53] offset:10240
	s_waitcnt vmcnt(29)
	ds_write_b128 v176, v[54:57] offset:15360
	s_waitcnt vmcnt(28)
	ds_write_b128 v176, v[58:61] offset:20480
	s_waitcnt vmcnt(27)
	ds_write_b128 v176, v[62:65] offset:25600
	s_waitcnt vmcnt(26)
	ds_write_b128 v176, v[66:69] offset:30720
	s_waitcnt vmcnt(25)
	ds_write_b128 v176, v[70:73] offset:35840
	s_waitcnt lgkmcnt(0)
	s_barrier
; #define LAS __attribute__((address_space(3)))
; #define XG_STEP(t_, PBN, PAN, PBS, PAS) do { XG_ISSUE_A(PAN, (t_) + 2); { const int tb_ = ((t_) + 3 < NK) ? (t_) + 3 : NK - 1; XG_ISSUE_B(PBN, tb_); } \
;                 XG_STORE(PBS, PAS, (((t_) + 1) & 1) * XG_BUF); __syncthreads(); } while (0)
; template <bool UP>
; __device__ __forceinline__ void xgemm_unit(const Args& a, LAS unsigned char* lds, int e, int s, int cnt, int off_e, int rp, int tid, int lane, int wave) {
;     ...
; #pragma unroll
;             for (int t = 0; t + 3 <= NK - 2; t += 3) {
;                 XG_STEP(t, pb0, pa2, pb1, pa1);
;                 if (!UP && t == 0) rw_ = RW[ras_];
;                 XG_STEP(t + 1, pb1, pa0, pb2, pa2);
;                 XG_STEP(t + 2, pb2, pa1, pb0, pa0);
;                 if (!UP && t == 0) { LAS int* ri_ = (LAS int*)(lds + 2 * XG_BUF + 2048); ri_[2 * tl] = ras_; ri_[2 * tl + 1] = __float_as_int(rw_); }
	buffer_load_dwordx4 v[10:13], v2, s[8:11], s27 offen
	buffer_load_dwordx4 v[14:17], v3, s[8:11], s27 offen
	s_waitcnt vmcnt(26)
	v_cvt_pk_bf16_f32 v74, v74, v75
	v_cvt_pk_bf16_f32 v75, v76, v77
	buffer_load_dwordx4 v[18:21], v4, s[8:11], s27 offen
	buffer_load_dwordx4 v[22:25], v5, s[8:11], s27 offen
	buffer_load_dwordx4 v[26:29], v6, s[8:11], s27 offen
	buffer_load_dwordx4 v[30:33], v7, s[8:11], s27 offen
	buffer_load_dwordx4 v[34:37], v8, s[8:11], s27 offen
	buffer_load_dwordx4 v[38:41], v9, s[8:11], s27 offen
	buffer_load_dwordx4 v[42:45], v181, s[12:15], s30 offen
	buffer_load_dwordx4 v[46:49], v181, s[12:15], s31 offen
	buffer_load_dwordx4 v[50:53], v181, s[12:15], s33 offen
	buffer_load_dwordx4 v[54:57], v181, s[12:15], s34 offen
	buffer_load_dwordx4 v[58:61], v181, s[12:15], s35 offen
	buffer_load_dwordx4 v[62:65], v181, s[12:15], s36 offen
	buffer_load_dwordx4 v[66:69], v181, s[12:15], s37 offen
	buffer_load_dwordx4 v[70:73], v181, s[12:15], s38 offen
	ds_write_b64 v155, v[74:75] offset:58368
	s_waitcnt vmcnt(39)
	v_cvt_pk_bf16_f32 v74, v78, v79
	v_cvt_pk_bf16_f32 v75, v80, v81
	ds_write_b64 v155, v[74:75] offset:60544
	s_waitcnt vmcnt(37)
	v_cvt_pk_bf16_f32 v74, v82, v83
	v_cvt_pk_bf16_f32 v75, v84, v85
	ds_write_b64 v155, v[74:75] offset:62720
	s_waitcnt vmcnt(34)
	v_cvt_pk_bf16_f32 v74, v94, v95
	v_cvt_pk_bf16_f32 v75, v96, v97
	ds_write_b64 v155, v[74:75] offset:64896
	s_waitcnt vmcnt(31)
	v_cvt_pk_bf16_f32 v74, v106, v107
	v_cvt_pk_bf16_f32 v75, v108, v109
	ds_write_b64 v156, v[74:75]
	s_waitcnt vmcnt(28)
	v_cvt_pk_bf16_f32 v74, v118, v119
	v_cvt_pk_bf16_f32 v75, v120, v121
	v_ashrrev_i32_e32 v229, 31, v228
	ds_write_b64 v157, v[74:75]
	s_waitcnt vmcnt(25)
	v_cvt_pk_bf16_f32 v74, v186, v187
	v_cvt_pk_bf16_f32 v75, v188, v189
	ds_write_b64 v158, v[74:75]
	s_waitcnt vmcnt(24)
	v_cvt_pk_bf16_f32 v74, v190, v191
	v_cvt_pk_bf16_f32 v75, v192, v193
	v_lshl_add_u64 v[126:127], v[228:229], 2, s[18:19]
	ds_write_b64 v159, v[74:75]
	ds_write_b128 v176, v[86:89] offset:58368
	ds_write_b128 v176, v[90:93] offset:63488
	ds_write_b128 v177, v[98:101] offset:58368
	ds_write_b128 v177, v[102:105] offset:63488
	ds_write_b128 v178, v[110:113] offset:58368
	ds_write_b128 v178, v[114:117] offset:63488
	ds_write_b128 v179, v[122:125] offset:58368
	ds_write_b128 v179, v[182:185] offset:63488
	s_waitcnt lgkmcnt(0)
	s_barrier
	buffer_load_dwordx4 v[74:77], v2, s[8:11], s39 offen
	buffer_load_dwordx4 v[78:81], v3, s[8:11], s39 offen
	buffer_load_dwordx4 v[82:85], v4, s[8:11], s39 offen
	buffer_load_dwordx4 v[86:89], v5, s[8:11], s39 offen
	buffer_load_dwordx4 v[90:93], v6, s[8:11], s39 offen
	buffer_load_dwordx4 v[94:97], v7, s[8:11], s39 offen
	buffer_load_dwordx4 v[98:101], v8, s[8:11], s39 offen
	buffer_load_dwordx4 v[102:105], v9, s[8:11], s39 offen
	buffer_load_dwordx4 v[106:109], v181, s[12:15], s40 offen
	buffer_load_dwordx4 v[110:113], v181, s[12:15], s41 offen
	buffer_load_dwordx4 v[114:117], v181, s[12:15], s42 offen
	buffer_load_dwordx4 v[118:121], v181, s[12:15], s43 offen
	buffer_load_dwordx4 v[122:125], v181, s[12:15], s44 offen
	buffer_load_dwordx4 v[182:185], v181, s[12:15], s45 offen
	buffer_load_dwordx4 v[186:189], v181, s[12:15], s46 offen
	buffer_load_dwordx4 v[190:193], v181, s[12:15], s47 offen
	global_load_dword v229, v[126:127], off
	s_waitcnt vmcnt(39)
	v_cvt_pk_bf16_f32 v126, v198, v199
	v_cvt_pk_bf16_f32 v127, v200, v201
	ds_write_b64 v154, v[126:127] offset:43136
	s_waitcnt vmcnt(38)
	v_cvt_pk_bf16_f32 v126, v202, v203
	v_cvt_pk_bf16_f32 v127, v204, v205
	ds_write_b64 v154, v[126:127] offset:45312
	s_waitcnt vmcnt(37)
	v_cvt_pk_bf16_f32 v126, v206, v207
	v_cvt_pk_bf16_f32 v127, v208, v209
	ds_write_b64 v154, v[126:127] offset:47488
	s_waitcnt vmcnt(36)
	v_cvt_pk_bf16_f32 v126, v210, v211
	v_cvt_pk_bf16_f32 v127, v212, v213
	ds_write_b64 v154, v[126:127] offset:49664
	s_waitcnt vmcnt(35)
	v_cvt_pk_bf16_f32 v126, v214, v215
	v_cvt_pk_bf16_f32 v127, v216, v217
	ds_write_b64 v154, v[126:127] offset:51840
	s_waitcnt vmcnt(34)
	v_cvt_pk_bf16_f32 v126, v218, v219
	v_cvt_pk_bf16_f32 v127, v220, v221
	v_cvt_pk_bf16_f32 v194, v194, v195
	v_cvt_pk_bf16_f32 v195, v196, v197
	ds_write_b64 v154, v[126:127] offset:54016
	s_waitcnt vmcnt(33)
	v_cvt_pk_bf16_f32 v126, v222, v223
	v_cvt_pk_bf16_f32 v127, v224, v225
	ds_write_b64 v154, v[194:195] offset:40960
	ds_write_b64 v154, v[126:127] offset:56192
	s_waitcnt vmcnt(32)
	ds_write_b128 v176, v[10:13]
	s_waitcnt vmcnt(31)
	ds_write_b128 v176, v[14:17] offset:5120
	s_waitcnt vmcnt(30)
	ds_write_b128 v176, v[18:21] offset:10240
	s_waitcnt vmcnt(29)
	ds_write_b128 v176, v[22:25] offset:15360
	s_waitcnt vmcnt(28)
	ds_write_b128 v176, v[26:29] offset:20480
	s_waitcnt vmcnt(27)
	ds_write_b128 v176, v[30:33] offset:25600
	s_waitcnt vmcnt(26)
	ds_write_b128 v176, v[34:37] offset:30720
	s_waitcnt vmcnt(25)
	ds_write_b128 v176, v[38:41] offset:35840
	s_waitcnt lgkmcnt(0)
	s_barrier
; #define LAS __attribute__((address_space(3)))
; #define XG_STEP(t_, PBN, PAN, PBS, PAS) do { XG_ISSUE_A(PAN, (t_) + 2); { const int tb_ = ((t_) + 3 < NK) ? (t_) + 3 : NK - 1; XG_ISSUE_B(PBN, tb_); } \
;                 XG_STORE(PBS, PAS, (((t_) + 1) & 1) * XG_BUF); __syncthreads(); } while (0)
; template <bool UP>
; __device__ __forceinline__ void xgemm_unit(const Args& a, LAS unsigned char* lds, int e, int s, int cnt, int off_e, int rp, int tid, int lane, int wave) {
;     ...
; #pragma unroll
;             for (int t = 0; t + 3 <= NK - 2; t += 3) {
;                 XG_STEP(t, pb0, pa2, pb1, pa1);
;                 if (!UP && t == 0) rw_ = RW[ras_];
;                 XG_STEP(t + 1, pb1, pa0, pb2, pa2);
;                 XG_STEP(t + 2, pb2, pa1, pb0, pa0);
;                 if (!UP && t == 0) { LAS int* ri_ = (LAS int*)(lds + 2 * XG_BUF + 2048); ri_[2 * tl] = ras_; ri_[2 * tl + 1] = __float_as_int(rw_); }
;             }
	buffer_load_dwordx4 v[10:13], v2, s[8:11], s48 offen
	buffer_load_dwordx4 v[14:17], v3, s[8:11], s48 offen
	buffer_load_dwordx4 v[18:21], v4, s[8:11], s48 offen
	buffer_load_dwordx4 v[22:25], v5, s[8:11], s48 offen
	buffer_load_dwordx4 v[26:29], v6, s[8:11], s48 offen
	buffer_load_dwordx4 v[30:33], v7, s[8:11], s48 offen
	buffer_load_dwordx4 v[34:37], v8, s[8:11], s48 offen
	buffer_load_dwordx4 v[38:41], v9, s[8:11], s48 offen
	buffer_load_dwordx4 v[194:197], v181, s[12:15], s49 offen
	buffer_load_dwordx4 v[198:201], v181, s[12:15], s50 offen
	buffer_load_dwordx4 v[202:205], v181, s[12:15], s51 offen
	buffer_load_dwordx4 v[206:209], v181, s[12:15], s52 offen
	buffer_load_dwordx4 v[210:213], v181, s[12:15], s53 offen
	buffer_load_dwordx4 v[214:217], v181, s[12:15], s60 offen
	buffer_load_dwordx4 v[218:221], v181, s[12:15], s61 offen
	buffer_load_dwordx4 v[222:225], v181, s[12:15], s62 offen
	s_waitcnt vmcnt(40)
	v_cvt_pk_bf16_f32 v42, v42, v43
	v_cvt_pk_bf16_f32 v43, v44, v45
	ds_write_b64 v155, v[42:43] offset:58368
	s_waitcnt vmcnt(39)
	v_cvt_pk_bf16_f32 v42, v46, v47
	v_cvt_pk_bf16_f32 v43, v48, v49
	ds_write_b64 v155, v[42:43] offset:60544
	s_waitcnt vmcnt(38)
	v_cvt_pk_bf16_f32 v42, v50, v51
	v_cvt_pk_bf16_f32 v43, v52, v53
	ds_write_b64 v155, v[42:43] offset:62720
	s_waitcnt vmcnt(37)
	v_cvt_pk_bf16_f32 v42, v54, v55
	v_cvt_pk_bf16_f32 v43, v56, v57
	ds_write_b64 v155, v[42:43] offset:64896
	s_waitcnt vmcnt(36)
	v_cvt_pk_bf16_f32 v42, v58, v59
	v_cvt_pk_bf16_f32 v43, v60, v61
	ds_write_b64 v156, v[42:43]
	s_waitcnt vmcnt(35)
	v_cvt_pk_bf16_f32 v42, v62, v63
	v_cvt_pk_bf16_f32 v43, v64, v65
	ds_write_b64 v157, v[42:43]
	s_waitcnt vmcnt(34)
	v_cvt_pk_bf16_f32 v42, v66, v67
	v_cvt_pk_bf16_f32 v43, v68, v69
	ds_write_b64 v158, v[42:43]
	s_waitcnt vmcnt(33)
	v_cvt_pk_bf16_f32 v42, v70, v71
	v_cvt_pk_bf16_f32 v43, v72, v73
	ds_write_b64 v159, v[42:43]
	s_waitcnt vmcnt(32)
	ds_write_b128 v176, v[74:77] offset:58368
	s_waitcnt vmcnt(31)
	ds_write_b128 v176, v[78:81] offset:63488
	s_waitcnt vmcnt(30)
	ds_write_b128 v177, v[82:85] offset:58368
	s_waitcnt vmcnt(29)
	ds_write_b128 v177, v[86:89] offset:63488
	s_waitcnt vmcnt(28)
	ds_write_b128 v178, v[90:93] offset:58368
	s_waitcnt vmcnt(27)
	ds_write_b128 v178, v[94:97] offset:63488
	s_waitcnt vmcnt(26)
	ds_write_b128 v179, v[98:101] offset:58368
	s_waitcnt vmcnt(25)
	ds_write_b128 v179, v[102:105] offset:63488
	s_waitcnt lgkmcnt(0)
	s_barrier
	s_waitcnt vmcnt(16)
	ds_write_b64 v180, v[228:229]
	buffer_load_dwordx4 v[42:45], v2, s[8:11], s63 offen
	buffer_load_dwordx4 v[46:49], v3, s[8:11], s63 offen
	buffer_load_dwordx4 v[50:53], v4, s[8:11], s63 offen
	buffer_load_dwordx4 v[54:57], v5, s[8:11], s63 offen
	buffer_load_dwordx4 v[58:61], v6, s[8:11], s63 offen
	buffer_load_dwordx4 v[62:65], v7, s[8:11], s63 offen
	buffer_load_dwordx4 v[66:69], v8, s[8:11], s63 offen
	buffer_load_dwordx4 v[70:73], v9, s[8:11], s63 offen
	buffer_load_dwordx4 v[74:77], v181, s[12:15], s64 offen
	buffer_load_dwordx4 v[78:81], v181, s[12:15], s65 offen
	buffer_load_dwordx4 v[82:85], v181, s[12:15], s66 offen
	buffer_load_dwordx4 v[86:89], v181, s[12:15], s67 offen
	buffer_load_dwordx4 v[90:93], v181, s[12:15], s68 offen
	buffer_load_dwordx4 v[94:97], v181, s[12:15], s69 offen
	buffer_load_dwordx4 v[98:101], v181, s[12:15], s70 offen
	buffer_load_dwordx4 v[102:105], v181, s[12:15], s71 offen
	v_cvt_pk_bf16_f32 v0, v106, v107
	v_cvt_pk_bf16_f32 v1, v108, v109
	ds_write_b64 v154, v[0:1] offset:40960
	v_cvt_pk_bf16_f32 v0, v110, v111
	v_cvt_pk_bf16_f32 v1, v112, v113
	ds_write_b64 v154, v[0:1] offset:43136
	v_cvt_pk_bf16_f32 v0, v114, v115
	v_cvt_pk_bf16_f32 v1, v116, v117
	ds_write_b64 v154, v[0:1] offset:45312
	v_cvt_pk_bf16_f32 v0, v118, v119
	v_cvt_pk_bf16_f32 v1, v120, v121
	ds_write_b64 v154, v[0:1] offset:47488
	v_cvt_pk_bf16_f32 v0, v122, v123
	v_cvt_pk_bf16_f32 v1, v124, v125
	ds_write_b64 v154, v[0:1] offset:49664
	v_cvt_pk_bf16_f32 v0, v182, v183
	v_cvt_pk_bf16_f32 v1, v184, v185
	ds_write_b64 v154, v[0:1] offset:51840
	v_cvt_pk_bf16_f32 v0, v186, v187
	v_cvt_pk_bf16_f32 v1, v188, v189
	ds_write_b64 v154, v[0:1] offset:54016
	v_cvt_pk_bf16_f32 v0, v190, v191
	v_cvt_pk_bf16_f32 v1, v192, v193
	ds_write_b64 v154, v[0:1] offset:56192
	s_waitcnt vmcnt(31)
	ds_write_b128 v176, v[10:13]
	s_waitcnt vmcnt(30)
	ds_write_b128 v176, v[14:17] offset:5120
	s_waitcnt vmcnt(29)
	ds_write_b128 v176, v[18:21] offset:10240
	s_waitcnt vmcnt(28)
	ds_write_b128 v176, v[22:25] offset:15360
	s_waitcnt vmcnt(27)
	ds_write_b128 v176, v[26:29] offset:20480
	s_waitcnt vmcnt(26)
	ds_write_b128 v176, v[30:33] offset:25600
	s_waitcnt vmcnt(25)
	ds_write_b128 v176, v[34:37] offset:30720
	s_waitcnt vmcnt(24)
	ds_write_b128 v176, v[38:41] offset:35840
	s_waitcnt vmcnt(23)
	v_cvt_pk_bf16_f32 v0, v194, v195
	v_cvt_pk_bf16_f32 v1, v196, v197
	s_waitcnt lgkmcnt(0)
	s_barrier
; #define LAS __attribute__((address_space(3)))
; #define XG_STORE(pb_, pa_, bo_) do { _Pragma("unroll") for (int j_ = 0; j_ < 8; ++j_) *(LAS v2u*)(lds + (bo_) + bdst + 8 * j_ * XG_BP) = pk4(pb_[j_]); \
;             _Pragma("unroll") for (int j_ = 0; j_ < 8; ++j_) *(LAS v4u*)(lds + (bo_) + (arow + 32 * j_) * XG_AP + ach * 16) = pa_[j_]; } while (0)
; #define XG_STEP(t_, PBN, PAN, PBS, PAS) do { XG_ISSUE_A(PAN, (t_) + 2); { const int tb_ = ((t_) + 3 < NK) ? (t_) + 3 : NK - 1; XG_ISSUE_B(PBN, tb_); } \
;                 XG_STORE(PBS, PAS, (((t_) + 1) & 1) * XG_BUF); __syncthreads(); } while (0)
; template <bool UP>
; __device__ __forceinline__ void xgemm_unit(const Args& a, LAS unsigned char* lds, int e, int s, int cnt, int off_e, int rp, int tid, int lane, int wave) {
;     ...
; #pragma unroll
;             for (int t = 0; t + 3 <= NK - 2; t += 3) {
;                 XG_STEP(t, pb0, pa2, pb1, pa1);
;                 if (!UP && t == 0) rw_ = RW[ras_];
;                 XG_STEP(t + 1, pb1, pa0, pb2, pa2);
;                 XG_STEP(t + 2, pb2, pa1, pb0, pa0);
;                 if (!UP && t == 0) { LAS int* ri_ = (LAS int*)(lds + 2 * XG_BUF + 2048); ri_[2 * tl] = ras_; ri_[2 * tl + 1] = __float_as_int(rw_); }
;             }
;             XG_STORE(pb1, pa1, ((NK - 1) & 1) * XG_BUF); __syncthreads();
;             __syncthreads();
	buffer_load_dwordx4 v[10:13], v2, s[8:11], s72 offen
	buffer_load_dwordx4 v[14:17], v3, s[8:11], s72 offen
	buffer_load_dwordx4 v[18:21], v4, s[8:11], s72 offen
	buffer_load_dwordx4 v[22:25], v5, s[8:11], s72 offen
	buffer_load_dwordx4 v[26:29], v6, s[8:11], s72 offen
	buffer_load_dwordx4 v[30:33], v7, s[8:11], s72 offen
	buffer_load_dwordx4 v[34:37], v8, s[8:11], s72 offen
	buffer_load_dwordx4 v[38:41], v9, s[8:11], s72 offen
	buffer_load_dwordx4 v[106:109], v181, s[12:15], s73 offen
	buffer_load_dwordx4 v[110:113], v181, s[12:15], s74 offen
	buffer_load_dwordx4 v[114:117], v181, s[12:15], s75 offen
	buffer_load_dwordx4 v[118:121], v181, s[12:15], s76 offen
	buffer_load_dwordx4 v[122:125], v181, s[12:15], s77 offen
	buffer_load_dwordx4 v[182:185], v181, s[12:15], s78 offen
	buffer_load_dwordx4 v[186:189], v181, s[12:15], s79 offen
	buffer_load_dwordx4 v[190:193], v181, s[12:15], s80 offen
	ds_write_b64 v155, v[0:1] offset:58368
	s_waitcnt vmcnt(38)
	v_cvt_pk_bf16_f32 v0, v198, v199
	v_cvt_pk_bf16_f32 v1, v200, v201
	ds_write_b64 v155, v[0:1] offset:60544
	s_waitcnt vmcnt(37)
	v_cvt_pk_bf16_f32 v0, v202, v203
	v_cvt_pk_bf16_f32 v1, v204, v205
	ds_write_b64 v155, v[0:1] offset:62720
	s_waitcnt vmcnt(36)
	v_cvt_pk_bf16_f32 v0, v206, v207
	v_cvt_pk_bf16_f32 v1, v208, v209
	ds_write_b64 v155, v[0:1] offset:64896
	s_waitcnt vmcnt(35)
	v_cvt_pk_bf16_f32 v0, v210, v211
	v_cvt_pk_bf16_f32 v1, v212, v213
	ds_write_b64 v156, v[0:1]
	s_waitcnt vmcnt(34)
	v_cvt_pk_bf16_f32 v0, v214, v215
	v_cvt_pk_bf16_f32 v1, v216, v217
	ds_write_b64 v157, v[0:1]
	s_waitcnt vmcnt(33)
	v_cvt_pk_bf16_f32 v0, v218, v219
	v_cvt_pk_bf16_f32 v1, v220, v221
	ds_write_b64 v158, v[0:1]
	s_waitcnt vmcnt(32)
	v_cvt_pk_bf16_f32 v0, v222, v223
	v_cvt_pk_bf16_f32 v1, v224, v225
	ds_write_b64 v159, v[0:1]
	s_waitcnt vmcnt(31)
	ds_write_b128 v176, v[42:45] offset:58368
	s_waitcnt vmcnt(30)
	ds_write_b128 v176, v[46:49] offset:63488
	s_waitcnt vmcnt(29)
	ds_write_b128 v177, v[50:53] offset:58368
	s_waitcnt vmcnt(28)
	ds_write_b128 v177, v[54:57] offset:63488
	s_waitcnt vmcnt(27)
	ds_write_b128 v178, v[58:61] offset:58368
	s_waitcnt vmcnt(26)
	ds_write_b128 v178, v[62:65] offset:63488
	s_waitcnt vmcnt(25)
	ds_write_b128 v179, v[66:69] offset:58368
	s_waitcnt vmcnt(24)
	ds_write_b128 v179, v[70:73] offset:63488
	s_waitcnt lgkmcnt(0)
	s_barrier
	buffer_load_dwordx4 v[42:45], v2, s[8:11], s81 offen
	s_nop 0
	buffer_load_dwordx4 v[0:3], v3, s[8:11], s81 offen
	s_nop 0
	buffer_load_dwordx4 v[46:49], v4, s[8:11], s81 offen
	buffer_load_dwordx4 v[50:53], v5, s[8:11], s81 offen
	buffer_load_dwordx4 v[54:57], v6, s[8:11], s81 offen
	s_nop 0
	buffer_load_dwordx4 v[4:7], v7, s[8:11], s81 offen
	s_nop 0
	buffer_load_dwordx4 v[58:61], v8, s[8:11], s81 offen
	buffer_load_dwordx4 v[62:65], v9, s[8:11], s81 offen
	s_waitcnt vmcnt(31)
	v_cvt_pk_bf16_f32 v8, v74, v75
	v_cvt_pk_bf16_f32 v9, v76, v77
	ds_write_b64 v154, v[8:9] offset:40960
	s_waitcnt vmcnt(30)
	v_cvt_pk_bf16_f32 v8, v78, v79
	v_cvt_pk_bf16_f32 v9, v80, v81
	ds_write_b64 v154, v[8:9] offset:43136
	s_waitcnt vmcnt(29)
	v_cvt_pk_bf16_f32 v8, v82, v83
	v_cvt_pk_bf16_f32 v9, v84, v85
	ds_write_b64 v154, v[8:9] offset:45312
	s_waitcnt vmcnt(28)
	v_cvt_pk_bf16_f32 v8, v86, v87
	v_cvt_pk_bf16_f32 v9, v88, v89
	ds_write_b64 v154, v[8:9] offset:47488
	s_waitcnt vmcnt(27)
	v_cvt_pk_bf16_f32 v8, v90, v91
	v_cvt_pk_bf16_f32 v9, v92, v93
	ds_write_b64 v154, v[8:9] offset:49664
	s_waitcnt vmcnt(26)
	v_cvt_pk_bf16_f32 v8, v94, v95
	v_cvt_pk_bf16_f32 v9, v96, v97
	ds_write_b64 v154, v[8:9] offset:51840
	s_waitcnt vmcnt(25)
	v_cvt_pk_bf16_f32 v8, v98, v99
	v_cvt_pk_bf16_f32 v9, v100, v101
	ds_write_b64 v154, v[8:9] offset:54016
	s_waitcnt vmcnt(24)
	v_cvt_pk_bf16_f32 v8, v102, v103
	v_cvt_pk_bf16_f32 v9, v104, v105
	ds_write_b64 v154, v[8:9] offset:56192
	s_waitcnt vmcnt(23)
	ds_write_b128 v176, v[10:13]
	s_waitcnt vmcnt(22)
	ds_write_b128 v176, v[14:17] offset:5120
	s_waitcnt vmcnt(21)
	ds_write_b128 v176, v[18:21] offset:10240
	s_waitcnt vmcnt(20)
	ds_write_b128 v176, v[22:25] offset:15360
	s_waitcnt vmcnt(19)
	ds_write_b128 v176, v[26:29] offset:20480
	s_waitcnt vmcnt(18)
	ds_write_b128 v176, v[30:33] offset:25600
	s_waitcnt vmcnt(17)
	ds_write_b128 v176, v[34:37] offset:30720
	s_waitcnt vmcnt(16)
	ds_write_b128 v176, v[38:41] offset:35840
	s_waitcnt vmcnt(15)
	v_cvt_pk_bf16_f32 v8, v106, v107
	v_cvt_pk_bf16_f32 v9, v108, v109
	v_add_u32_e32 v10, 0, v153
	s_waitcnt lgkmcnt(0)
	s_barrier
	ds_write_b64 v10, v[8:9] offset:58368
	s_waitcnt vmcnt(14)
	v_cvt_pk_bf16_f32 v8, v110, v111
	v_cvt_pk_bf16_f32 v9, v112, v113
	ds_write_b64 v10, v[8:9] offset:60544
	s_waitcnt vmcnt(13)
	v_cvt_pk_bf16_f32 v8, v114, v115
	v_cvt_pk_bf16_f32 v9, v116, v117
	ds_write_b64 v10, v[8:9] offset:62720
	s_waitcnt vmcnt(12)
	v_cvt_pk_bf16_f32 v8, v118, v119
	v_cvt_pk_bf16_f32 v9, v120, v121
	ds_write_b64 v10, v[8:9] offset:64896
	s_waitcnt vmcnt(11)
	v_cvt_pk_bf16_f32 v8, v122, v123
	v_cvt_pk_bf16_f32 v9, v124, v125
	v_add_u32_e32 v10, s0, v153
	ds_write_b64 v10, v[8:9] offset:8704
	s_waitcnt vmcnt(10)
	v_cvt_pk_bf16_f32 v8, v182, v183
	v_cvt_pk_bf16_f32 v9, v184, v185
	ds_write_b64 v10, v[8:9] offset:10880
	s_waitcnt vmcnt(9)
	v_cvt_pk_bf16_f32 v8, v186, v187
	v_cvt_pk_bf16_f32 v9, v188, v189
	ds_write_b64 v10, v[8:9] offset:13056
	s_waitcnt vmcnt(8)
	v_cvt_pk_bf16_f32 v8, v190, v191
	v_cvt_pk_bf16_f32 v9, v192, v193
	ds_write_b64 v10, v[8:9] offset:15232
	s_waitcnt vmcnt(7)
	ds_write_b128 v176, v[42:45] offset:58368
	s_waitcnt vmcnt(6)
	ds_write_b128 v176, v[0:3] offset:63488
	s_waitcnt vmcnt(5)
	ds_write_b128 v177, v[46:49] offset:58368
	s_waitcnt vmcnt(4)
	ds_write_b128 v177, v[50:53] offset:63488
	s_waitcnt vmcnt(3)
	ds_write_b128 v178, v[54:57] offset:58368
	s_waitcnt vmcnt(2)
	ds_write_b128 v178, v[4:7] offset:63488
	s_waitcnt vmcnt(1)
	ds_write_b128 v179, v[58:61] offset:58368
	s_waitcnt vmcnt(0)
	ds_write_b128 v179, v[62:65] offset:63488
	s_waitcnt lgkmcnt(0)
	s_barrier
; template <bool UP>
; __device__ __forceinline__ void xgemm_unit(const Args& a, LAS unsigned char* lds, int e, int s, int cnt, int off_e, int rp, int tid, int lane, int wave) {
;     ...
;         const int nrows = (cnt - rp < XG_RM) ? (cnt - rp) : XG_RM;
;         if (loader) {
;             const int tl = tid & 255;
;             const int arow = tl >> 3, ach = tl & 7;
;             const int n4 = UP ? (tl & 15) : (tl & 31), kr = UP ? ((tl >> 4) & 7) : (tl >> 5), bcol = UP ? (64 * ((wave >> 1) & 1) + 4 * n4) : 4 * n4;
;             const float* Bu = UP ? ((((wave >> 1) & 1) ? a.in[I_W3] : a.in[I_W1]) + (size_t)e * D * DE) : (a.in[I_W2] + (size_t)e * DE * D);
;             const __amdgpu_buffer_rsrc_t rB = __builtin_amdgcn_make_buffer_rsrc((void*)Bu, (short)0, K * LDB * 4, 0x00020000);
;             const __amdgpu_buffer_rsrc_t rA = __builtin_amdgcn_make_buffer_rsrc((void*)Abase, (short)0, UP ? T * D * 2 : 2 * T * DE * 2, 0x00020000);
;             const unsigned boff = (unsigned)(kr * LDB + 4 * n4 + (UP ? 64 : 128) * s) * 4u;
;             const int bdst = XG_ABYTES + kr * XG_BP + bcol * 2;
;             unsigned aoff[8];
; #pragma unroll
;             for (int j = 0; j < 8; ++j) { int rr = arow + 32 * j; rr = (rr < nrows) ? rr : (nrows - 1);
;                 if (UP) aoff[j] = ((unsigned)(LISTS[rp + rr] >> 1) * (unsigned)D + ach * 8) * 2u; else aoff[j] = ((unsigned)(off_e + rp + rr) * (unsigned)DE + ach * 8) * 2u; }
;             f32x4 pb0[8], pb1[8], pb2[8]; v4u pa0[8], pa1[8], pa2[8];
;             static_assert(NK % 3 == 2, "loader ring schedule");
;     ...
;             __builtin_amdgcn_s_setprio(1);
;             int ras_ = 0; float rw_ = 0.f;
;             if (!UP) ras_ = LISTS[rp + ((tl < nrows) ? tl : nrows - 1)];
;             XG_ISSUE_A(pa0, 0); XG_ISSUE_B(pb0, 0); XG_ISSUE_A(pa1, 1); XG_ISSUE_B(pb1, 1); XG_ISSUE_B(pb2, 2);
; template <bool UP>
; __device__ __forceinline__ void xgemm_phase(const Args& a, LAS unsigned char* lds, int tid, int lane, int wave) {
;     ...
;     for (int u = vcu; u < nitem; u += G) { const int ep = __builtin_amdgcn_readfirstlane(eptab[u >> SH]); const int e = ep & 255, rp = (ep >> 8) * XG_RM, s = u & ((1 << SH) - 1);
;         xgemm_unit<UP>(a, lds, e, s, __builtin_amdgcn_readfirstlane(cnts[e]), __builtin_amdgcn_readfirstlane(offs[e]), rp, tid, lane, wave); }
	s_mov_b32 s100, 0
	s_add_i32 s20, s3, s2
	s_cmp_lt_i32 s20, s22
	s_cbranch_scc0 .Lxd_nonext
	s_ashr_i32 s0, s20, 4
	s_lshl_b32 s0, s0, 2
	s_add_i32 s0, s0, 0
	s_add_i32 s0, s0, 0x1ca10
	v_mov_b32_e32 v0, s0
	ds_read_b32 v0, v0
	s_and_b32 s83, s20, 15
	s_waitcnt lgkmcnt(0)
	v_readfirstlane_b32 s0, v0
	s_and_b32 s12, s0, 0xff
	s_and_b32 s82, s0, 0xffffff00
	s_lshl_b32 s0, s12, 2
	s_add_i32 s0, s0, 0
	s_add_i32 s1, s0, 0x1c800
	v_mov_b32_e32 v0, s1
	ds_read_b32 v0, v0
	s_add_i32 s0, s0, 0x1c900
	s_waitcnt lgkmcnt(0)
	v_readfirstlane_b32 s1, v0
	v_mov_b32_e32 v0, s0
	ds_read_b32 v0, v0
	s_sub_i32 s84, s1, s82
	s_min_i32 s86, s84, 0x100
	s_waitcnt lgkmcnt(0)
	v_readfirstlane_b32 s85, v0
	s_lshl_b32 s0, s12, 15
	s_add_u32 s0, s25, s0
	s_addc_u32 s1, s26, 0
	s_lshl_b32 s12, s12, 22
	s_add_u32 s12, s54, s12
	s_addc_u32 s13, s55, 0
	s_add_i32 s20, s86, -1
	s_add_i32 s85, s85, s82
	v_min_i32_e32 v0, s20, v144
	v_add_u32_e32 v0, s85, v0
	v_lshl_or_b32 v2, v0, 10, v145
	v_min_i32_e32 v0, s20, v146
	v_add_u32_e32 v0, s85, v0
	v_lshl_or_b32 v3, v0, 10, v145
	v_min_i32_e32 v0, s20, v147
	v_add_u32_e32 v0, s85, v0
	v_lshl_or_b32 v4, v0, 10, v145
	v_min_i32_e32 v0, s20, v148
	v_add_u32_e32 v0, s85, v0
	v_lshl_or_b32 v5, v0, 10, v145
	v_min_i32_e32 v0, s20, v149
	v_add_u32_e32 v0, s85, v0
	v_lshl_or_b32 v6, v0, 10, v145
	v_min_i32_e32 v0, s20, v150
	v_add_u32_e32 v0, s85, v0
	v_lshl_or_b32 v7, v0, 10, v145
	v_min_i32_e32 v0, s20, v151
	v_add_u32_e32 v0, s85, v0
	v_lshl_or_b32 v8, v0, 10, v145
	v_min_i32_e32 v0, s20, v152
	v_add_u32_e32 v0, s85, v0
	s_and_b32 s13, s13, 0xffff
	v_lshl_or_b32 v9, v0, 10, v145
	s_setprio 1
	v_lshl_or_b32 v181, s83, 9, v174
	s_mov_b32 s83, 0x10000
	buffer_load_dwordx4 v[10:13], v181, s[12:15], 0 offen
	buffer_load_dwordx4 v[14:17], v181, s[12:15], s83 offen
	buffer_load_dwordx4 v[18:21], v181, s[12:15], s15 offen
	s_mov_b32 s83, 0x30000
	v_mov_b32_e32 v0, s20
	v_cmp_gt_i32_e32 vcc, s84, v143
	buffer_load_dwordx4 v[22:25], v181, s[12:15], s83 offen
	s_mov_b32 s83, 0x40000
	v_cndmask_b32_e32 v0, v0, v143, vcc
	buffer_load_dwordx4 v[26:29], v181, s[12:15], s83 offen
	s_mov_b32 s83, 0x50000
	v_add_u32_e32 v0, s82, v0
	buffer_load_dwordx4 v[30:33], v181, s[12:15], s83 offen
	s_mov_b32 s83, 0x60000
	v_ashrrev_i32_e32 v1, 31, v0
	buffer_load_dwordx4 v[34:37], v181, s[12:15], s83 offen
	s_mov_b32 s83, 0x70000
	v_lshl_add_u64 v[0:1], v[0:1], 2, s[0:1]
	s_mov_b32 s0, 0x80000
	buffer_load_dwordx4 v[38:41], v181, s[12:15], s83 offen
	buffer_load_dwordx4 v[42:45], v2, s[8:11], 0 offen
	buffer_load_dwordx4 v[46:49], v3, s[8:11], 0 offen
	buffer_load_dwordx4 v[50:53], v4, s[8:11], 0 offen
	buffer_load_dwordx4 v[54:57], v5, s[8:11], 0 offen
	buffer_load_dwordx4 v[58:61], v6, s[8:11], 0 offen
	buffer_load_dwordx4 v[62:65], v7, s[8:11], 0 offen
	buffer_load_dwordx4 v[66:69], v8, s[8:11], 0 offen
	buffer_load_dwordx4 v[70:73], v9, s[8:11], 0 offen
	buffer_load_dwordx4 v[74:77], v181, s[12:15], s0 offen
	s_mov_b32 s0, 0x90000
	buffer_load_dwordx4 v[78:81], v181, s[12:15], s0 offen
	s_mov_b32 s0, 0xa0000
	global_load_dword v228, v[0:1], off
	s_nop 0
	buffer_load_dwordx4 v[82:85], v181, s[12:15], s0 offen
	buffer_load_dwordx4 v[86:89], v2, s[8:11], s24 offen
	buffer_load_dwordx4 v[90:93], v3, s[8:11], s24 offen
	s_mov_b32 s0, 0xb0000
	buffer_load_dwordx4 v[94:97], v181, s[12:15], s0 offen
	buffer_load_dwordx4 v[98:101], v4, s[8:11], s24 offen
	buffer_load_dwordx4 v[102:105], v5, s[8:11], s24 offen
	s_mov_b32 s0, 0xc0000
	buffer_load_dwordx4 v[106:109], v181, s[12:15], s0 offen
	buffer_load_dwordx4 v[110:113], v6, s[8:11], s24 offen
	buffer_load_dwordx4 v[114:117], v7, s[8:11], s24 offen
	s_mov_b32 s0, 0xd0000
	buffer_load_dwordx4 v[118:121], v181, s[12:15], s0 offen
	buffer_load_dwordx4 v[122:125], v8, s[8:11], s24 offen
	buffer_load_dwordx4 v[182:185], v9, s[8:11], s24 offen
	s_mov_b32 s0, 0xe0000
	buffer_load_dwordx4 v[186:189], v181, s[12:15], s0 offen
	s_mov_b32 s0, 0xf0000
	buffer_load_dwordx4 v[190:193], v181, s[12:15], s0 offen
	s_mov_b32 s0, 0x100000
	buffer_load_dwordx4 v[194:197], v181, s[12:15], s0 offen
	s_mov_b32 s0, 0x110000
	buffer_load_dwordx4 v[198:201], v181, s[12:15], s0 offen
	s_mov_b32 s0, 0x120000
	buffer_load_dwordx4 v[202:205], v181, s[12:15], s0 offen
	s_mov_b32 s0, 0x130000
	buffer_load_dwordx4 v[206:209], v181, s[12:15], s0 offen
	s_mov_b32 s0, 0x140000
	buffer_load_dwordx4 v[210:213], v181, s[12:15], s0 offen
	s_mov_b32 s0, 0x150000
	buffer_load_dwordx4 v[214:217], v181, s[12:15], s0 offen
	buffer_load_dwordx4 v[218:221], v181, s[12:15], s28 offen
	buffer_load_dwordx4 v[222:225], v181, s[12:15], s29 offen
	s_mov_b32 s98, s12
	s_mov_b32 s99, s13
	s_mov_b32 s100, 1
.Lxd_nonext:
	s_barrier
	s_setprio 0
	s_branch .LBB0_1263

; __global__ void __launch_bounds__(NTHR, 2) fwd_kernel(Args args) {
;     extern __shared__ __attribute__((aligned(16))) unsigned char lds_raw[];
	.amdhsa_kernel _Z10fwd_kernel4Args
		.amdhsa_group_segment_fixed_size 0
		.amdhsa_private_segment_fixed_size 0
		.amdhsa_kernarg_size 456
		.amdhsa_user_sgpr_count 2
		.amdhsa_user_sgpr_dispatch_ptr 0
		.amdhsa_user_sgpr_queue_ptr 0
		.amdhsa_user_sgpr_kernarg_segment_ptr 1
		.amdhsa_user_sgpr_dispatch_id 0
		.amdhsa_user_sgpr_kernarg_preload_length 0
		.amdhsa_user_sgpr_kernarg_preload_offset 0
		.amdhsa_user_sgpr_private_segment_size 0
		.amdhsa_uses_dynamic_stack 0
		.amdhsa_enable_private_segment 0
		.amdhsa_system_sgpr_workgroup_id_x 1
		.amdhsa_system_sgpr_workgroup_id_y 0
		.amdhsa_system_sgpr_workgroup_id_z 0
		.amdhsa_system_sgpr_workgroup_info 0
		.amdhsa_system_vgpr_workitem_id 0
		.amdhsa_next_free_vgpr 245
		.amdhsa_next_free_sgpr 102
		.amdhsa_accum_offset 248
		.amdhsa_reserve_vcc 1
		.amdhsa_float_round_mode_32 0
		.amdhsa_float_round_mode_16_64 0
		.amdhsa_float_denorm_mode_32 3
		.amdhsa_float_denorm_mode_16_64 3
		.amdhsa_dx10_clamp 1
		.amdhsa_ieee_mode 1
		.amdhsa_fp16_overflow 0
		.amdhsa_tg_split 0
		.amdhsa_exception_fp_ieee_invalid_op 0
		.amdhsa_exception_fp_denorm_src 0
		.amdhsa_exception_fp_ieee_div_zero 0
		.amdhsa_exception_fp_ieee_overflow 0
		.amdhsa_exception_fp_ieee_underflow 0
		.amdhsa_exception_fp_ieee_inexact 0
		.amdhsa_exception_int_div_zero 0
	.end_amdhsa_kernel

; __global__ void __launch_bounds__(NTHR, 2) fwd_kernel(Args args) {
;     extern __shared__ __attribute__((aligned(16))) unsigned char lds_raw[];
amdhsa.kernels:
  - .agpr_count:     0
    .args:
      - .offset:         0
        .size:           200
        .value_kind:     by_value
      - .offset:         200
        .size:           4
        .value_kind:     hidden_block_count_x
      - .offset:         204
        .size:           4
        .value_kind:     hidden_block_count_y
      - .offset:         208
        .size:           4
        .value_kind:     hidden_block_count_z
      - .offset:         212
        .size:           2
        .value_kind:     hidden_group_size_x
      - .offset:         214
        .size:           2
        .value_kind:     hidden_group_size_y
      - .offset:         216
        .size:           2
        .value_kind:     hidden_group_size_z
      - .offset:         218
        .size:           2
        .value_kind:     hidden_remainder_x
      - .offset:         220
        .size:           2
        .value_kind:     hidden_remainder_y
      - .offset:         222
        .size:           2
        .value_kind:     hidden_remainder_z
      - .offset:         240
        .size:           8
        .value_kind:     hidden_global_offset_x
      - .offset:         248
        .size:           8
        .value_kind:     hidden_global_offset_y
      - .offset:         256
        .size:           8
        .value_kind:     hidden_global_offset_z
      - .offset:         264
        .size:           2
        .value_kind:     hidden_grid_dims
      - .offset:         320
        .size:           4
        .value_kind:     hidden_dynamic_lds_size
    .group_segment_fixed_size: 0
    .kernarg_segment_align: 8
    .kernarg_segment_size: 456
    .language:       OpenCL C
    .language_version:
      - 2
      - 0
    .max_flat_workgroup_size: 512
    .name:           _Z10fwd_kernel4Args
    .private_segment_fixed_size: 0
    .sgpr_count:     108
    .sgpr_spill_count: 24
    .symbol:         _Z10fwd_kernel4Args.kd
    .uniform_work_group_size: 1
    .uses_dynamic_stack: false
    .vgpr_count:     245
    .vgpr_spill_count: 0
    .wavefront_size: 64
